# stack21 plus bf16 packing of the P operand whose f32 sources survive in v168..v175 moved from the softmax tail into the P.V section (behind the MFMA preceding its consumer)
# speedup vs baseline: 1.0039x; 1.0039x over previous
; DI void finishSM(f32x16& p0, f32x16& p1, float alpha, float& l_reg, bf16x8& pa0, bf16x8& pa1, bf16x8& pa2, bf16x8& pa3) {
; #pragma unroll
;     for (int r = 0; r < 16; ++r) p1[r] = __builtin_amdgcn_exp2f(p1[r]);
;     float ps = 0;
; #pragma unroll
;     for (int r = 0; r < 16; ++r) ps += p0[r];
; #pragma unroll
;     for (int r = 0; r < 16; ++r) ps += p1[r];
;     { auto rr = __builtin_amdgcn_permlane32_swap(__float_as_uint(ps), __float_as_uint(ps), false, false); ps = __uint_as_float(rr[0]) + __uint_as_float(rr[1]); }
;     l_reg = l_reg * alpha + ps;
;     ...
;     AT_PK4(p0, 0, pa0); AT_PK4(p0, 8, pa1); AT_PK4(p1, 0, pa2); AT_PK4(p1, 8, pa3);
;     ...
; }
; DI void qkt(f32x16& p0, f32x16& p1, const char* Ks, const bf16x8* qr, const f32x16& negm, int r32, int hi) {
; #pragma unroll
;     for (int d0 = 0; d0 < 4; ++d0) { const int cb = (d0 * 16 + hi * 8) * 2;
;         const bf16x8 b0 = *reinterpret_cast<const bf16x8*>(Ks + AT_KSWZ(r32, cb));
;         const bf16x8 b1 = *reinterpret_cast<const bf16x8*>(Ks + AT_KSWZ(32 + r32, cb));
;         p0 = __builtin_amdgcn_mfma_f32_32x32x16_bf16(b0, qr[d0], d0 == 0 ? negm : p0, 0, 0, 0);
;         p1 = __builtin_amdgcn_mfma_f32_32x32x16_bf16(b1, qr[d0], d0 == 0 ? negm : p1, 0, 0, 0); }
; }
; template <int D0> DI void pv_one(f32x16& od, int vb, bf16x8 pa0, bf16x8 pa1, bf16x8 pa2, bf16x8 pa3) {
;     const s16x4 l0 = tr_read<v_rd_off(D0, 0, 0)>(vb), h0 = tr_read<v_rd_off(D0, 0, 1)>(vb), l1 = tr_read<v_rd_off(D0, 1, 0)>(vb), h1 = tr_read<v_rd_off(D0, 1, 1)>(vb);
;     const s16x4 l2 = tr_read<v_rd_off(D0, 2, 0)>(vb), h2 = tr_read<v_rd_off(D0, 2, 1)>(vb), l3 = tr_read<v_rd_off(D0, 3, 0)>(vb), h3 = tr_read<v_rd_off(D0, 3, 1)>(vb);
;     asm volatile("s_waitcnt lgkmcnt(0)" ::: "memory"); AT_SBAR();
;     ...
;     od = __builtin_amdgcn_mfma_f32_32x32x16_bf16(AT_PK(l0, h0), pa0, od, 0, 0, 0);
;     od = __builtin_amdgcn_mfma_f32_32x32x16_bf16(AT_PK(l1, h1), pa1, od, 0, 0, 0);
;     od = __builtin_amdgcn_mfma_f32_32x32x16_bf16(AT_PK(l2, h2), pa2, od, 0, 0, 0);
;     od = __builtin_amdgcn_mfma_f32_32x32x16_bf16(AT_PK(l3, h3), pa3, od, 0, 0, 0);
;     ...
; }
; DI void pv_all_sm(f32x16* o, int vb, bf16x8 pa0, bf16x8 pa1, bf16x8 pa2, bf16x8 pa3, f32x16& p0, f32x16& p1, float& m_ref, f32x16& negm, float& alpha) {
;     pv_one<0>(o[0], vb, pa0, pa1, pa2, pa3);
;     float pmax = p0[0];
; #pragma unroll
;     for (int r = 1; r < 16; ++r) pmax = fmaxf(pmax, p0[r]);
.LBB4_702:
	s_lshl_b32 s26, s66, 13
	s_add_i32 s26, s26, 0
	v_add_u32_e32 v72, s26, v205
	v_add_u32_e32 v112, s26, v206
	v_add_u32_e32 v180, s26, v207
	s_waitcnt lgkmcnt(1)
	v_mfma_f32_32x32x16_bf16 v[128:143], v[64:67], v[156:159], v[80:95]
	ds_read_b128 v[64:67], v72 offset:49152
	ds_read_b128 v[72:75], v72 offset:53248
	ds_read_b128 v[76:79], v112 offset:49152
	ds_read_b128 v[220:223], v112 offset:53248
	v_exp_f32_e32 v186, v97
	v_exp_f32_e32 v213, v98
	v_exp_f32_e32 v214, v99
	v_exp_f32_e32 v219, v100
	v_exp_f32_e32 v228, v101
	s_waitcnt lgkmcnt(4)
	v_mfma_f32_32x32x16_bf16 v[112:127], v[68:71], v[156:159], v[80:95]
	ds_read_b128 v[68:71], v180 offset:49152
	ds_read_b128 v[224:227], v180 offset:53248
	v_exp_f32_e32 v180, v96
	v_cvt_pk_bf16_f32 v96, v216, v218
	v_cvt_pk_bf16_f32 v97, v179, v217
	v_cvt_pk_bf16_f32 v98, v177, v215
	v_cvt_pk_bf16_f32 v99, v176, v178
	s_waitcnt lgkmcnt(4)
	v_mfma_f32_32x32x16_bf16 v[112:127], v[72:75], v[152:155], v[112:127]
	v_add_f32_e32 v75, 0, v216
	v_add_f32_e32 v75, v218, v75
	v_add_f32_e32 v75, v217, v75
	v_add_f32_e32 v75, v215, v75
	v_add_f32_e32 v75, v176, v75
	v_mfma_f32_32x32x16_bf16 v[128:143], v[64:67], v[152:155], v[128:143]
	v_add_f32_e32 v75, v172, v75
	s_waitcnt lgkmcnt(3)
	v_mfma_f32_32x32x16_bf16 v[128:143], v[76:79], v[148:151], v[128:143]
	v_add_f32_e32 v75, v180, v75
	v_add_f32_e32 v75, v186, v75
	v_exp_f32_e32 v64, v102
	v_exp_f32_e32 v65, v103
	v_exp_f32_e32 v66, v104
	s_waitcnt lgkmcnt(2)
	v_mfma_f32_32x32x16_bf16 v[112:127], v[220:223], v[148:151], v[112:127]
	v_exp_f32_e32 v67, v105
	v_exp_f32_e32 v105, v106
	v_exp_f32_e32 v106, v107
	v_exp_f32_e32 v107, v108
	v_exp_f32_e32 v72, v109
	v_exp_f32_e32 v73, v110
	v_exp_f32_e32 v74, v111
	s_waitcnt lgkmcnt(1)
	v_mfma_f32_32x32x16_bf16 v[128:143], v[68:71], v[144:147], v[128:143]
	v_add_f32_e32 v68, v213, v75
	v_add_f32_e32 v68, v214, v68
	v_add_f32_e32 v68, v219, v68
	v_add_f32_e32 v68, v228, v68
	v_add_f32_e32 v68, v64, v68
	v_add_f32_e32 v68, v65, v68
	v_add_f32_e32 v68, v66, v68
	v_add_f32_e32 v68, v67, v68
	s_waitcnt lgkmcnt(0)
	v_mfma_f32_32x32x16_bf16 v[112:127], v[224:227], v[144:147], v[112:127]
	v_add_f32_e32 v68, v105, v68
	v_add_f32_e32 v68, v106, v68
	v_add_f32_e32 v68, v107, v68
	v_add_f32_e32 v68, v72, v68
	v_add_f32_e32 v68, v73, v68
	v_add_f32_e32 v183, v74, v68
	v_cvt_pk_bf16_f32 v100, v180, v186
	v_cvt_pk_bf16_f32 v101, v213, v214
	v_cvt_pk_bf16_f32 v102, v219, v228
	v_cvt_pk_bf16_f32 v103, v64, v65
	v_cvt_pk_bf16_f32 v104, v66, v67
	v_cvt_pk_bf16_f32 v105, v105, v106
	v_cvt_pk_bf16_f32 v106, v107, v72
	v_cvt_pk_bf16_f32 v107, v73, v74
	s_add_u32 s74, s46, s28
	s_addc_u32 s75, s47, s29
	s_add_u32 s78, s74, 0x23808000
	s_addc_u32 s79, s75, 0
	s_add_u32 s80, s74, 0x2380a000
	s_addc_u32 s81, s75, 0
	s_add_u32 s76, s46, s30
	s_addc_u32 s77, s47, s31
	s_add_u32 s82, s76, 0x21804000
	s_addc_u32 s83, s77, 0
	s_lshl_b32 s92, s64, 14
	s_add_i32 s92, s92, s94
	s_mov_b32 m0, s92
	s_lshl_b32 s96, s64, 13
	global_load_lds_dwordx4 v249, s[78:79]
	s_addk_i32 s92, 0x400
	s_mov_b32 m0, s92
	s_add_i32 s96, s96, s95
	global_load_lds_dwordx4 v250, s[78:79]
	s_nop 0
	s_mov_b32 m0, s96
	s_nop 0
	global_load_lds_dwordx4 v251, s[82:83]
	s_andn2_b64 vcc, exec, s[2:3]
	s_cbranch_vccnz .LBB4_704
	s_mov_b64 s[2:3], s[8:9]
	global_store_dwordx2 v189, v[184:185], s[2:3] nt
.LBB4_704:
	s_lshl_b32 s67, s65, 14
	v_add_u32_e32 v186, s67, v253
	ds_read_b64_tr_b16 v[64:65], v186 offset:0
	ds_read_b64_tr_b16 v[66:67], v186 offset:0x100
	ds_read_b64_tr_b16 v[68:69], v186 offset:0x1000
	ds_read_b64_tr_b16 v[70:71], v186 offset:0x1100
	ds_read_b64_tr_b16 v[72:73], v186 offset:0x2000
	ds_read_b64_tr_b16 v[74:75], v186 offset:0x2100
	ds_read_b64_tr_b16 v[76:77], v186 offset:0x3000
	ds_read_b64_tr_b16 v[78:79], v186 offset:0x3100
	s_waitcnt lgkmcnt(0)
	v_mfma_f32_32x32x16_bf16 v[32:47], v[64:67], v[96:99], v[32:47]
	v_cvt_pk_bf16_f32 v108, v173, v175
	v_cvt_pk_bf16_f32 v109, v171, v174
	v_cvt_pk_bf16_f32 v110, v169, v172
	v_cvt_pk_bf16_f32 v111, v168, v170
	v_max_f32_e32 v64, v128, v129
	v_max3_f32 v64, v64, v130, v131
	v_max3_f32 v64, v64, v132, v133
	v_max3_f32 v64, v64, v134, v135
	v_max3_f32 v64, v64, v136, v137
	v_mfma_f32_32x32x16_bf16 v[32:47], v[68:71], v[108:111], v[32:47]
	v_max3_f32 v64, v64, v138, v139
	v_max3_f32 v66, v64, v140, v141
	ds_read_b64_tr_b16 v[64:65], v186 offset:0x200
	v_max3_f32 v180, v66, v142, v143
	ds_read_b64_tr_b16 v[66:67], v186 offset:0x300
	ds_read_b64_tr_b16 v[68:69], v186 offset:0x1200
	ds_read_b64_tr_b16 v[70:71], v186 offset:0x1300
	v_mfma_f32_32x32x16_bf16 v[32:47], v[72:75], v[100:103], v[32:47]
	v_add_f32_e32 v254, v179, v177
	v_add_f32_e32 v254, v178, v254
	ds_read_b64_tr_b16 v[72:73], v186 offset:0x2200
	ds_read_b64_tr_b16 v[74:75], v186 offset:0x2300
	ds_read_b64_tr_b16 v[214:215], v186 offset:0x3200
	ds_read_b64_tr_b16 v[216:217], v186 offset:0x3300
	v_mfma_f32_32x32x16_bf16 v[32:47], v[76:79], v[104:107], v[32:47]
	v_add_f32_e32 v254, v173, v254
	v_add_f32_e32 v254, v175, v254
	s_waitcnt lgkmcnt(0)
	v_mfma_f32_32x32x16_bf16 v[48:63], v[64:67], v[96:99], v[48:63]
	v_add_f32_e32 v254, v171, v254
	v_add_f32_e32 v254, v174, v254
	v_max3_f32 v76, v180, v112, v113
	v_max3_f32 v64, v76, v114, v115
	ds_read_b64_tr_b16 v[66:67], v186 offset:0x400
	v_max3_f32 v64, v64, v116, v117
	v_max3_f32 v64, v64, v118, v119
	v_max3_f32 v64, v64, v120, v121
	v_max3_f32 v64, v64, v122, v123
	v_mfma_f32_32x32x16_bf16 v[48:63], v[68:71], v[108:111], v[48:63]
	v_add_f32_e32 v254, v169, v254
	v_add_f32_e32 v254, v168, v254
	ds_read_b64_tr_b16 v[68:69], v186 offset:0x500
	ds_read_b64_tr_b16 v[70:71], v186 offset:0x1400
	v_max3_f32 v64, v64, v124, v125
	v_max3_f32 v64, v64, v126, v127
	v_mov_b32_e32 v65, v64
	s_nop 1
	v_permlane32_swap_b32_e32 v64, v65
	v_mfma_f32_32x32x16_bf16 v[48:63], v[72:75], v[100:103], v[48:63]
	ds_read_b64_tr_b16 v[72:73], v186 offset:0x1500
	ds_read_b64_tr_b16 v[74:75], v186 offset:0x2400
	ds_read_b64_tr_b16 v[76:77], v186 offset:0x2500
	ds_read_b64_tr_b16 v[218:219], v186 offset:0x3400
	ds_read_b64_tr_b16 v[220:221], v186 offset:0x3500
	v_mfma_f32_32x32x16_bf16 v[48:63], v[214:217], v[104:107], v[48:63]
	s_waitcnt lgkmcnt(0)
	v_max_f32_e32 v64, v64, v65
	v_mfma_f32_32x32x16_bf16 v[16:31], v[66:69], v[96:99], v[16:31]
	v_cmp_ge_f32_e32 vcc, s25, v64
	s_cmp_eq_u64 vcc, exec
	v_mfma_f32_32x32x16_bf16 v[16:31], v[70:73], v[108:111], v[16:31]
	v_mfma_f32_32x32x16_bf16 v[16:31], v[74:77], v[100:103], v[16:31]
	v_mfma_f32_32x32x16_bf16 v[16:31], v[218:221], v[104:107], v[16:31]
	s_cbranch_scc0 .LBB4_737
	v_mov_b32_e32 v180, 1.0

; DI void finishSM(f32x16& p0, f32x16& p1, float alpha, float& l_reg, bf16x8& pa0, bf16x8& pa1, bf16x8& pa2, bf16x8& pa3) {
; #pragma unroll
;     for (int r = 0; r < 16; ++r) p1[r] = __builtin_amdgcn_exp2f(p1[r]);
;     float ps = 0;
; #pragma unroll
;     for (int r = 0; r < 16; ++r) ps += p0[r];
; #pragma unroll
;     for (int r = 0; r < 16; ++r) ps += p1[r];
;     { auto rr = __builtin_amdgcn_permlane32_swap(__float_as_uint(ps), __float_as_uint(ps), false, false); ps = __uint_as_float(rr[0]) + __uint_as_float(rr[1]); }
;     l_reg = l_reg * alpha + ps;
;     ...
;     AT_PK4(p0, 0, pa0); AT_PK4(p0, 8, pa1); AT_PK4(p1, 0, pa2); AT_PK4(p1, 8, pa3);
;     ...
; }
; DI void qkt(f32x16& p0, f32x16& p1, const char* Ks, const bf16x8* qr, const f32x16& negm, int r32, int hi) {
; #pragma unroll
;     for (int d0 = 0; d0 < 4; ++d0) { const int cb = (d0 * 16 + hi * 8) * 2;
;         const bf16x8 b0 = *reinterpret_cast<const bf16x8*>(Ks + AT_KSWZ(r32, cb));
;         const bf16x8 b1 = *reinterpret_cast<const bf16x8*>(Ks + AT_KSWZ(32 + r32, cb));
;         p0 = __builtin_amdgcn_mfma_f32_32x32x16_bf16(b0, qr[d0], d0 == 0 ? negm : p0, 0, 0, 0);
;         p1 = __builtin_amdgcn_mfma_f32_32x32x16_bf16(b1, qr[d0], d0 == 0 ? negm : p1, 0, 0, 0); }
; }
; template <int D0> DI void pv_one(f32x16& od, int vb, bf16x8 pa0, bf16x8 pa1, bf16x8 pa2, bf16x8 pa3) {
;     const s16x4 l0 = tr_read<v_rd_off(D0, 0, 0)>(vb), h0 = tr_read<v_rd_off(D0, 0, 1)>(vb), l1 = tr_read<v_rd_off(D0, 1, 0)>(vb), h1 = tr_read<v_rd_off(D0, 1, 1)>(vb);
;     const s16x4 l2 = tr_read<v_rd_off(D0, 2, 0)>(vb), h2 = tr_read<v_rd_off(D0, 2, 1)>(vb), l3 = tr_read<v_rd_off(D0, 3, 0)>(vb), h3 = tr_read<v_rd_off(D0, 3, 1)>(vb);
;     asm volatile("s_waitcnt lgkmcnt(0)" ::: "memory"); AT_SBAR();
;     ...
;     od = __builtin_amdgcn_mfma_f32_32x32x16_bf16(AT_PK(l0, h0), pa0, od, 0, 0, 0);
;     od = __builtin_amdgcn_mfma_f32_32x32x16_bf16(AT_PK(l1, h1), pa1, od, 0, 0, 0);
;     od = __builtin_amdgcn_mfma_f32_32x32x16_bf16(AT_PK(l2, h2), pa2, od, 0, 0, 0);
;     od = __builtin_amdgcn_mfma_f32_32x32x16_bf16(AT_PK(l3, h3), pa3, od, 0, 0, 0);
;     ...
; }
; DI void pv_all_sm(f32x16* o, int vb, bf16x8 pa0, bf16x8 pa1, bf16x8 pa2, bf16x8 pa3, f32x16& p0, f32x16& p1, float& m_ref, f32x16& negm, float& alpha) {
;     pv_one<0>(o[0], vb, pa0, pa1, pa2, pa3);
;     float pmax = p0[0];
; #pragma unroll
;     for (int r = 1; r < 16; ++r) pmax = fmaxf(pmax, p0[r]);
.LBB4_723:
	v_exp_f32_e32 v186, v128
	v_exp_f32_e32 v230, v129
	v_exp_f32_e32 v231, v130
	v_exp_f32_e32 v232, v131
	v_exp_f32_e32 v233, v132
	v_exp_f32_e32 v234, v133
	v_exp_f32_e32 v235, v134
	v_exp_f32_e32 v236, v135
	v_exp_f32_e32 v237, v136
	v_exp_f32_e32 v238, v137
	v_exp_f32_e32 v239, v138
	v_exp_f32_e32 v240, v139
	v_exp_f32_e32 v241, v140
	v_exp_f32_e32 v242, v141
	v_exp_f32_e32 v243, v142
	v_exp_f32_e32 v244, v143
	v_add_u32_e32 v101, s78, v205
	v_add_u32_e32 v102, s78, v206
	v_add_u32_e32 v103, s78, v207
	ds_read_b128 v[172:175], v101 offset:49152
	ds_read_b128 v[176:179], v101 offset:53248
	ds_read_b128 v[214:217], v102 offset:49152
	ds_read_b128 v[218:221], v102 offset:53248
	ds_read_b128 v[222:225], v103 offset:49152
	ds_read_b128 v[226:229], v103 offset:53248
	v_exp_f32_e32 v112, v112
	v_exp_f32_e32 v113, v113
	v_exp_f32_e32 v114, v114
	s_waitcnt lgkmcnt(7)
	v_mfma_f32_32x32x16_bf16 v[128:143], v[96:99], v[156:159], v[80:95]
	v_exp_f32_e32 v115, v115
	v_exp_f32_e32 v116, v116
	v_exp_f32_e32 v117, v117
	v_exp_f32_e32 v118, v118
	v_exp_f32_e32 v119, v119
	s_waitcnt lgkmcnt(6)
	v_mfma_f32_32x32x16_bf16 v[96:111], v[168:171], v[156:159], v[80:95]
	v_exp_f32_e32 v168, v120
	v_add_f32_e32 v120, 0, v186
	v_add_f32_e32 v120, v230, v120
	v_add_f32_e32 v120, v231, v120
	v_add_f32_e32 v120, v232, v120
	v_add_f32_e32 v120, v233, v120
	v_add_f32_e32 v120, v234, v120
	v_add_f32_e32 v120, v235, v120
	v_add_f32_e32 v120, v236, v120
	v_add_f32_e32 v120, v237, v120
	v_add_f32_e32 v120, v238, v120
	s_waitcnt lgkmcnt(5)
	v_mfma_f32_32x32x16_bf16 v[128:143], v[172:175], v[152:155], v[128:143]
	v_add_f32_e32 v120, v239, v120
	v_add_f32_e32 v120, v240, v120
	v_add_f32_e32 v120, v241, v120
	v_add_f32_e32 v120, v242, v120
	v_add_f32_e32 v120, v243, v120
	v_add_f32_e32 v120, v244, v120
	v_add_f32_e32 v120, v112, v120
	s_waitcnt lgkmcnt(4)
	v_mfma_f32_32x32x16_bf16 v[96:111], v[176:179], v[152:155], v[96:111]
	v_add_f32_e32 v120, v113, v120
	v_add_f32_e32 v120, v114, v120
	v_add_f32_e32 v120, v115, v120
	v_add_f32_e32 v120, v116, v120
	v_exp_f32_e32 v169, v121
	v_add_f32_e32 v120, v117, v120
	v_exp_f32_e32 v170, v122
	s_waitcnt lgkmcnt(3)
	v_mfma_f32_32x32x16_bf16 v[128:143], v[214:217], v[148:151], v[128:143]
	v_add_f32_e32 v120, v118, v120
	v_exp_f32_e32 v171, v123
	v_add_f32_e32 v120, v119, v120
	v_exp_f32_e32 v172, v124
	v_exp_f32_e32 v173, v125
	s_waitcnt lgkmcnt(2)
	v_mfma_f32_32x32x16_bf16 v[96:111], v[218:221], v[148:151], v[96:111]
	v_exp_f32_e32 v174, v126
	v_exp_f32_e32 v175, v127
	v_add_f32_e32 v120, v174, v120
	s_waitcnt lgkmcnt(1)
	v_mfma_f32_32x32x16_bf16 v[128:143], v[222:225], v[144:147], v[128:143]
	v_add_f32_e32 v213, v175, v120
	v_cvt_pk_bf16_f32 v120, v186, v230
	v_cvt_pk_bf16_f32 v121, v231, v232
	v_cvt_pk_bf16_f32 v122, v233, v234
	v_cvt_pk_bf16_f32 v123, v235, v236
	v_cvt_pk_bf16_f32 v124, v237, v238
	s_waitcnt lgkmcnt(0)
	v_mfma_f32_32x32x16_bf16 v[96:111], v[226:229], v[144:147], v[96:111]
	v_cvt_pk_bf16_f32 v125, v239, v240
	v_cvt_pk_bf16_f32 v126, v241, v242
	v_cvt_pk_bf16_f32 v127, v243, v244
	v_cvt_pk_bf16_f32 v112, v112, v113
	v_cvt_pk_bf16_f32 v113, v114, v115
	v_cvt_pk_bf16_f32 v114, v116, v117
	v_cvt_pk_bf16_f32 v115, v118, v119
	s_add_u32 s78, s74, 0x2380c000
	s_addc_u32 s79, s75, 0
	s_add_u32 s74, s74, 0x2380e000
	s_addc_u32 s75, s75, 0
	s_add_u32 s76, s76, 0x21806000
	s_addc_u32 s77, s77, 0
	s_lshl_b32 s92, s65, 14
	s_add_i32 s92, s92, s94
	s_mov_b32 m0, s92
	s_lshl_b32 s96, s65, 13
	global_load_lds_dwordx4 v249, s[78:79]
	s_addk_i32 s92, 0x400
	s_mov_b32 m0, s92
	s_add_i32 s96, s96, s95
	global_load_lds_dwordx4 v250, s[78:79]
	s_nop 0
	s_mov_b32 m0, s96
	s_nop 0
	global_load_lds_dwordx4 v251, s[76:77]
	s_nop 0
	s_and_b64 vcc, exec, s[2:3]
	s_cbranch_vccnz .LBB4_725
	s_mov_b64 s[2:3], s[8:9]
	global_store_dwordx2 v189, v[184:185], s[2:3] nt
.LBB4_725:
	v_lshl_add_u32 v215, s66, 14, v253
	ds_read_b64_tr_b16 v[216:217], v215 offset:0
	ds_read_b64_tr_b16 v[218:219], v215 offset:0x100
	ds_read_b64_tr_b16 v[220:221], v215 offset:0x1000
	ds_read_b64_tr_b16 v[222:223], v215 offset:0x1100
	ds_read_b64_tr_b16 v[224:225], v215 offset:0x2000
	ds_read_b64_tr_b16 v[226:227], v215 offset:0x2100
	ds_read_b64_tr_b16 v[228:229], v215 offset:0x3000
	ds_read_b64_tr_b16 v[230:231], v215 offset:0x3100
	s_waitcnt lgkmcnt(0)
	v_mfma_f32_32x32x16_bf16 v[32:47], v[216:219], v[120:123], v[32:47]
	v_max_f32_e32 v186, v128, v129
	ds_read_b64_tr_b16 v[216:217], v215 offset:0x200
	ds_read_b64_tr_b16 v[218:219], v215 offset:0x300
	v_max3_f32 v186, v186, v130, v131
	v_max3_f32 v186, v186, v132, v133
	v_mfma_f32_32x32x16_bf16 v[32:47], v[220:223], v[124:127], v[32:47]
	ds_read_b64_tr_b16 v[220:221], v215 offset:0x1200
	ds_read_b64_tr_b16 v[222:223], v215 offset:0x1300
	v_max3_f32 v186, v186, v134, v135
	v_max3_f32 v186, v186, v136, v137
	v_max3_f32 v186, v186, v138, v139
	v_max3_f32 v186, v186, v140, v141
	v_max3_f32 v186, v186, v142, v143
	v_mfma_f32_32x32x16_bf16 v[32:47], v[224:227], v[112:115], v[32:47]
	v_cvt_pk_bf16_f32 v116, v168, v169
	v_cvt_pk_bf16_f32 v117, v170, v171
	v_cvt_pk_bf16_f32 v118, v172, v173
	v_cvt_pk_bf16_f32 v119, v174, v175
	v_add_f32_e32 v254, v168, v169
	v_add_f32_e32 v254, v170, v254
	ds_read_b64_tr_b16 v[224:225], v215 offset:0x2200
	ds_read_b64_tr_b16 v[226:227], v215 offset:0x2300
	ds_read_b64_tr_b16 v[232:233], v215 offset:0x3200
	ds_read_b64_tr_b16 v[234:235], v215 offset:0x3300
	v_mfma_f32_32x32x16_bf16 v[32:47], v[228:231], v[116:119], v[32:47]
	v_add_f32_e32 v254, v171, v254
	v_add_f32_e32 v254, v172, v254
	s_waitcnt lgkmcnt(0)
	v_mfma_f32_32x32x16_bf16 v[48:63], v[216:219], v[120:123], v[48:63]
	v_max3_f32 v186, v186, v96, v97
	v_max3_f32 v186, v186, v98, v99
	ds_read_b64_tr_b16 v[218:219], v215 offset:0x400
	v_max3_f32 v186, v186, v100, v101
	v_max3_f32 v186, v186, v102, v103
	v_max3_f32 v186, v186, v104, v105
	v_max3_f32 v186, v186, v106, v107
	v_mfma_f32_32x32x16_bf16 v[48:63], v[220:223], v[124:127], v[48:63]
	ds_read_b64_tr_b16 v[220:221], v215 offset:0x500
	ds_read_b64_tr_b16 v[222:223], v215 offset:0x1400
	v_max3_f32 v186, v186, v108, v109
	v_max3_f32 v186, v186, v110, v111
	v_mov_b32_e32 v216, v186
	s_nop 1
	v_permlane32_swap_b32_e32 v186, v216
	v_mfma_f32_32x32x16_bf16 v[48:63], v[224:227], v[112:115], v[48:63]
	ds_read_b64_tr_b16 v[224:225], v215 offset:0x1500
	ds_read_b64_tr_b16 v[226:227], v215 offset:0x2400
	ds_read_b64_tr_b16 v[228:229], v215 offset:0x2500
	ds_read_b64_tr_b16 v[236:237], v215 offset:0x3400
	ds_read_b64_tr_b16 v[238:239], v215 offset:0x3500
	v_mfma_f32_32x32x16_bf16 v[48:63], v[232:235], v[116:119], v[48:63]
	s_waitcnt lgkmcnt(0)
	v_max_f32_e32 v216, v186, v216
	v_mfma_f32_32x32x16_bf16 v[16:31], v[218:221], v[120:123], v[16:31]
	v_cmp_ge_f32_e32 vcc, s25, v216
	s_cmp_eq_u64 vcc, exec
	v_mov_b32_e32 v186, 1.0
	v_mfma_f32_32x32x16_bf16 v[16:31], v[222:225], v[124:127], v[16:31]
	v_mfma_f32_32x32x16_bf16 v[16:31], v[226:229], v[112:115], v[16:31]
	v_mfma_f32_32x32x16_bf16 v[16:31], v[236:239], v[116:119], v[16:31]
	s_cbranch_scc0 .LBB4_738

; DI void finishSM(f32x16& p0, f32x16& p1, float alpha, float& l_reg, bf16x8& pa0, bf16x8& pa1, bf16x8& pa2, bf16x8& pa3) {
; #pragma unroll
;     for (int r = 0; r < 16; ++r) p1[r] = __builtin_amdgcn_exp2f(p1[r]);
;     float ps = 0;
; #pragma unroll
;     for (int r = 0; r < 16; ++r) ps += p0[r];
; #pragma unroll
;     for (int r = 0; r < 16; ++r) ps += p1[r];
;     { auto rr = __builtin_amdgcn_permlane32_swap(__float_as_uint(ps), __float_as_uint(ps), false, false); ps = __uint_as_float(rr[0]) + __uint_as_float(rr[1]); }
;     l_reg = l_reg * alpha + ps;
;     ...
;     AT_PK4(p0, 0, pa0); AT_PK4(p0, 8, pa1); AT_PK4(p1, 0, pa2); AT_PK4(p1, 8, pa3);
;     ...
; }
; DI void qkt(f32x16& p0, f32x16& p1, const char* Ks, const bf16x8* qr, const f32x16& negm, int r32, int hi) {
; #pragma unroll
;     for (int d0 = 0; d0 < 4; ++d0) { const int cb = (d0 * 16 + hi * 8) * 2;
;         const bf16x8 b0 = *reinterpret_cast<const bf16x8*>(Ks + AT_KSWZ(r32, cb));
;         const bf16x8 b1 = *reinterpret_cast<const bf16x8*>(Ks + AT_KSWZ(32 + r32, cb));
;         p0 = __builtin_amdgcn_mfma_f32_32x32x16_bf16(b0, qr[d0], d0 == 0 ? negm : p0, 0, 0, 0);
;         p1 = __builtin_amdgcn_mfma_f32_32x32x16_bf16(b1, qr[d0], d0 == 0 ? negm : p1, 0, 0, 0); }
; }
; template <int D0> DI void pv_one(f32x16& od, int vb, bf16x8 pa0, bf16x8 pa1, bf16x8 pa2, bf16x8 pa3) {
;     const s16x4 l0 = tr_read<v_rd_off(D0, 0, 0)>(vb), h0 = tr_read<v_rd_off(D0, 0, 1)>(vb), l1 = tr_read<v_rd_off(D0, 1, 0)>(vb), h1 = tr_read<v_rd_off(D0, 1, 1)>(vb);
;     const s16x4 l2 = tr_read<v_rd_off(D0, 2, 0)>(vb), h2 = tr_read<v_rd_off(D0, 2, 1)>(vb), l3 = tr_read<v_rd_off(D0, 3, 0)>(vb), h3 = tr_read<v_rd_off(D0, 3, 1)>(vb);
;     asm volatile("s_waitcnt lgkmcnt(0)" ::: "memory"); AT_SBAR();
;     ...
;     od = __builtin_amdgcn_mfma_f32_32x32x16_bf16(AT_PK(l0, h0), pa0, od, 0, 0, 0);
;     od = __builtin_amdgcn_mfma_f32_32x32x16_bf16(AT_PK(l1, h1), pa1, od, 0, 0, 0);
;     od = __builtin_amdgcn_mfma_f32_32x32x16_bf16(AT_PK(l2, h2), pa2, od, 0, 0, 0);
;     od = __builtin_amdgcn_mfma_f32_32x32x16_bf16(AT_PK(l3, h3), pa3, od, 0, 0, 0);
;     ...
; }
; DI void pv_all_sm(f32x16* o, int vb, bf16x8 pa0, bf16x8 pa1, bf16x8 pa2, bf16x8 pa3, f32x16& p0, f32x16& p1, float& m_ref, f32x16& negm, float& alpha) {
;     pv_one<0>(o[0], vb, pa0, pa1, pa2, pa3);
;     float pmax = p0[0];
; #pragma unroll
;     for (int r = 1; r < 16; ++r) pmax = fmaxf(pmax, p0[r]);
.LBB4_775:
	s_lshl_b32 s20, s30, 13
	s_add_i32 s20, s20, 0
	v_add_u32_e32 v72, s20, v208
	v_add_u32_e32 v112, s20, v209
	v_add_u32_e32 v180, s20, v210
	s_waitcnt lgkmcnt(1)
	v_mfma_f32_32x32x16_bf16 v[128:143], v[64:67], v[156:159], v[80:95]
	ds_read_b128 v[64:67], v72 offset:49152
	ds_read_b128 v[72:75], v72 offset:53248
	ds_read_b128 v[76:79], v112 offset:49152
	ds_read_b128 v[224:227], v112 offset:53248
	v_exp_f32_e32 v182, v97
	v_exp_f32_e32 v217, v98
	v_exp_f32_e32 v218, v99
	v_exp_f32_e32 v223, v100
	v_exp_f32_e32 v232, v101
	s_waitcnt lgkmcnt(4)
	v_mfma_f32_32x32x16_bf16 v[112:127], v[68:71], v[156:159], v[80:95]
	ds_read_b128 v[68:71], v180 offset:49152
	ds_read_b128 v[228:231], v180 offset:53248
	v_exp_f32_e32 v180, v96
	v_cvt_pk_bf16_f32 v96, v220, v222
	v_cvt_pk_bf16_f32 v97, v179, v221
	v_cvt_pk_bf16_f32 v98, v177, v219
	v_cvt_pk_bf16_f32 v99, v176, v178
	s_waitcnt lgkmcnt(4)
	v_mfma_f32_32x32x16_bf16 v[112:127], v[72:75], v[152:155], v[112:127]
	v_add_f32_e32 v75, 0, v220
	v_add_f32_e32 v75, v222, v75
	v_add_f32_e32 v75, v221, v75
	v_add_f32_e32 v75, v219, v75
	v_add_f32_e32 v75, v176, v75
	v_mfma_f32_32x32x16_bf16 v[128:143], v[64:67], v[152:155], v[128:143]
	v_add_f32_e32 v75, v172, v75
	s_waitcnt lgkmcnt(3)
	v_mfma_f32_32x32x16_bf16 v[128:143], v[76:79], v[148:151], v[128:143]
	v_add_f32_e32 v75, v180, v75
	v_add_f32_e32 v75, v182, v75
	v_exp_f32_e32 v64, v102
	v_exp_f32_e32 v65, v103
	v_exp_f32_e32 v66, v104
	s_waitcnt lgkmcnt(2)
	v_mfma_f32_32x32x16_bf16 v[112:127], v[224:227], v[148:151], v[112:127]
	v_exp_f32_e32 v67, v105
	v_exp_f32_e32 v105, v106
	v_exp_f32_e32 v106, v107
	v_exp_f32_e32 v107, v108
	v_exp_f32_e32 v72, v109
	v_exp_f32_e32 v73, v110
	v_exp_f32_e32 v74, v111
	s_waitcnt lgkmcnt(1)
	v_mfma_f32_32x32x16_bf16 v[128:143], v[68:71], v[144:147], v[128:143]
	v_add_f32_e32 v68, v217, v75
	v_add_f32_e32 v68, v218, v68
	v_add_f32_e32 v68, v223, v68
	v_add_f32_e32 v68, v232, v68
	v_add_f32_e32 v68, v64, v68
	v_add_f32_e32 v68, v65, v68
	v_add_f32_e32 v68, v66, v68
	v_add_f32_e32 v68, v67, v68
	s_waitcnt lgkmcnt(0)
	v_mfma_f32_32x32x16_bf16 v[112:127], v[228:231], v[144:147], v[112:127]
	v_add_f32_e32 v68, v105, v68
	v_add_f32_e32 v68, v106, v68
	v_add_f32_e32 v68, v107, v68
	v_add_f32_e32 v68, v72, v68
	v_add_f32_e32 v68, v73, v68
	v_add_f32_e32 v215, v74, v68
	v_cvt_pk_bf16_f32 v100, v180, v182
	v_cvt_pk_bf16_f32 v101, v217, v218
	v_cvt_pk_bf16_f32 v102, v223, v232
	v_cvt_pk_bf16_f32 v103, v64, v65
	v_cvt_pk_bf16_f32 v104, v66, v67
	v_cvt_pk_bf16_f32 v105, v105, v106
	v_cvt_pk_bf16_f32 v106, v107, v72
	v_cvt_pk_bf16_f32 v107, v73, v74
	s_add_u32 s34, s46, s16
	s_addc_u32 s35, s47, s17
	s_add_u32 s24, s34, 0x23808000
	s_addc_u32 s25, s35, 0
	s_add_u32 s66, s34, 0x2380a000
	s_addc_u32 s67, s35, 0
	s_add_u32 s37, s46, s18
	s_addc_u32 s64, s47, s19
	s_add_u32 s74, s37, 0x21884000
	s_addc_u32 s75, s64, 0
	s_lshl_b32 s92, s15, 14
	s_add_i32 s92, s92, s94
	s_mov_b32 m0, s92
	s_lshl_b32 s96, s15, 13
	global_load_lds_dwordx4 v249, s[24:25]
	s_addk_i32 s92, 0x400
	s_mov_b32 m0, s92
	s_add_i32 s96, s96, s95
	global_load_lds_dwordx4 v250, s[24:25]
	s_nop 0
	s_mov_b32 m0, s96
	s_nop 0
	global_load_lds_dwordx4 v251, s[74:75]
	s_andn2_b64 vcc, exec, s[2:3]
	s_cbranch_vccnz .LBB4_777
	s_mov_b64 s[2:3], s[8:9]
	global_store_dwordx2 v193, v[184:185], s[2:3] nt
.LBB4_777:
	s_lshl_b32 s31, s29, 14
	v_add_u32_e32 v182, s31, v253
	ds_read_b64_tr_b16 v[64:65], v182 offset:0
	ds_read_b64_tr_b16 v[66:67], v182 offset:0x100
	ds_read_b64_tr_b16 v[68:69], v182 offset:0x1000
	ds_read_b64_tr_b16 v[70:71], v182 offset:0x1100
	ds_read_b64_tr_b16 v[72:73], v182 offset:0x2000
	ds_read_b64_tr_b16 v[74:75], v182 offset:0x2100
	ds_read_b64_tr_b16 v[76:77], v182 offset:0x3000
	ds_read_b64_tr_b16 v[78:79], v182 offset:0x3100
	s_waitcnt lgkmcnt(0)
	v_mfma_f32_32x32x16_bf16 v[48:63], v[64:67], v[96:99], v[48:63]
	v_cvt_pk_bf16_f32 v108, v173, v175
	v_cvt_pk_bf16_f32 v109, v171, v174
	v_cvt_pk_bf16_f32 v110, v169, v172
	v_cvt_pk_bf16_f32 v111, v168, v170
	v_max_f32_e32 v64, v128, v129
	v_max3_f32 v64, v64, v130, v131
	v_max3_f32 v64, v64, v132, v133
	v_max3_f32 v64, v64, v134, v135
	v_max3_f32 v64, v64, v136, v137
	v_mfma_f32_32x32x16_bf16 v[48:63], v[68:71], v[108:111], v[48:63]
	v_max3_f32 v64, v64, v138, v139
	v_max3_f32 v66, v64, v140, v141
	ds_read_b64_tr_b16 v[64:65], v182 offset:0x200
	v_max3_f32 v180, v66, v142, v143
	ds_read_b64_tr_b16 v[66:67], v182 offset:0x300
	ds_read_b64_tr_b16 v[68:69], v182 offset:0x1200
	ds_read_b64_tr_b16 v[70:71], v182 offset:0x1300
	v_mfma_f32_32x32x16_bf16 v[48:63], v[72:75], v[100:103], v[48:63]
	v_add_f32_e32 v254, v179, v177
	v_add_f32_e32 v254, v178, v254
	ds_read_b64_tr_b16 v[72:73], v182 offset:0x2200
	ds_read_b64_tr_b16 v[74:75], v182 offset:0x2300
	ds_read_b64_tr_b16 v[218:219], v182 offset:0x3200
	ds_read_b64_tr_b16 v[220:221], v182 offset:0x3300
	v_mfma_f32_32x32x16_bf16 v[48:63], v[76:79], v[104:107], v[48:63]
	v_add_f32_e32 v254, v173, v254
	v_add_f32_e32 v254, v175, v254
	s_waitcnt lgkmcnt(0)
	v_mfma_f32_32x32x16_bf16 v[32:47], v[64:67], v[96:99], v[32:47]
	v_add_f32_e32 v254, v171, v254
	v_add_f32_e32 v254, v174, v254
	v_max3_f32 v76, v180, v112, v113
	v_max3_f32 v64, v76, v114, v115
	ds_read_b64_tr_b16 v[66:67], v182 offset:0x400
	v_max3_f32 v64, v64, v116, v117
	v_max3_f32 v64, v64, v118, v119
	v_max3_f32 v64, v64, v120, v121
	v_max3_f32 v64, v64, v122, v123
	v_mfma_f32_32x32x16_bf16 v[32:47], v[68:71], v[108:111], v[32:47]
	v_add_f32_e32 v254, v169, v254
	v_add_f32_e32 v254, v168, v254
	ds_read_b64_tr_b16 v[68:69], v182 offset:0x500
	ds_read_b64_tr_b16 v[70:71], v182 offset:0x1400
	v_max3_f32 v64, v64, v124, v125
	v_max3_f32 v64, v64, v126, v127
	v_mov_b32_e32 v65, v64
	s_nop 1
	v_permlane32_swap_b32_e32 v64, v65
	v_mfma_f32_32x32x16_bf16 v[32:47], v[72:75], v[100:103], v[32:47]
	ds_read_b64_tr_b16 v[72:73], v182 offset:0x1500
	ds_read_b64_tr_b16 v[74:75], v182 offset:0x2400
	ds_read_b64_tr_b16 v[76:77], v182 offset:0x2500
	ds_read_b64_tr_b16 v[222:223], v182 offset:0x3400
	ds_read_b64_tr_b16 v[224:225], v182 offset:0x3500
	v_mfma_f32_32x32x16_bf16 v[32:47], v[218:221], v[104:107], v[32:47]
	s_waitcnt lgkmcnt(0)
	v_max_f32_e32 v64, v64, v65
	v_mfma_f32_32x32x16_bf16 v[16:31], v[66:69], v[96:99], v[16:31]
	v_cmp_ge_f32_e32 vcc, s26, v64
	s_cmp_eq_u64 vcc, exec
	v_mfma_f32_32x32x16_bf16 v[16:31], v[70:73], v[108:111], v[16:31]
	v_mfma_f32_32x32x16_bf16 v[16:31], v[74:77], v[100:103], v[16:31]
	v_mfma_f32_32x32x16_bf16 v[16:31], v[222:225], v[104:107], v[16:31]
	s_cbranch_scc0 .LBB4_810
	v_mov_b32_e32 v180, 1.0

; DI void finishSM(f32x16& p0, f32x16& p1, float alpha, float& l_reg, bf16x8& pa0, bf16x8& pa1, bf16x8& pa2, bf16x8& pa3) {
; #pragma unroll
;     for (int r = 0; r < 16; ++r) p1[r] = __builtin_amdgcn_exp2f(p1[r]);
;     float ps = 0;
; #pragma unroll
;     for (int r = 0; r < 16; ++r) ps += p0[r];
; #pragma unroll
;     for (int r = 0; r < 16; ++r) ps += p1[r];
;     { auto rr = __builtin_amdgcn_permlane32_swap(__float_as_uint(ps), __float_as_uint(ps), false, false); ps = __uint_as_float(rr[0]) + __uint_as_float(rr[1]); }
;     l_reg = l_reg * alpha + ps;
;     ...
;     AT_PK4(p0, 0, pa0); AT_PK4(p0, 8, pa1); AT_PK4(p1, 0, pa2); AT_PK4(p1, 8, pa3);
;     ...
; }
; DI void qkt(f32x16& p0, f32x16& p1, const char* Ks, const bf16x8* qr, const f32x16& negm, int r32, int hi) {
; #pragma unroll
;     for (int d0 = 0; d0 < 4; ++d0) { const int cb = (d0 * 16 + hi * 8) * 2;
;         const bf16x8 b0 = *reinterpret_cast<const bf16x8*>(Ks + AT_KSWZ(r32, cb));
;         const bf16x8 b1 = *reinterpret_cast<const bf16x8*>(Ks + AT_KSWZ(32 + r32, cb));
;         p0 = __builtin_amdgcn_mfma_f32_32x32x16_bf16(b0, qr[d0], d0 == 0 ? negm : p0, 0, 0, 0);
;         p1 = __builtin_amdgcn_mfma_f32_32x32x16_bf16(b1, qr[d0], d0 == 0 ? negm : p1, 0, 0, 0); }
; }
; template <int D0> DI void pv_one(f32x16& od, int vb, bf16x8 pa0, bf16x8 pa1, bf16x8 pa2, bf16x8 pa3) {
;     const s16x4 l0 = tr_read<v_rd_off(D0, 0, 0)>(vb), h0 = tr_read<v_rd_off(D0, 0, 1)>(vb), l1 = tr_read<v_rd_off(D0, 1, 0)>(vb), h1 = tr_read<v_rd_off(D0, 1, 1)>(vb);
;     const s16x4 l2 = tr_read<v_rd_off(D0, 2, 0)>(vb), h2 = tr_read<v_rd_off(D0, 2, 1)>(vb), l3 = tr_read<v_rd_off(D0, 3, 0)>(vb), h3 = tr_read<v_rd_off(D0, 3, 1)>(vb);
;     asm volatile("s_waitcnt lgkmcnt(0)" ::: "memory"); AT_SBAR();
;     ...
;     od = __builtin_amdgcn_mfma_f32_32x32x16_bf16(AT_PK(l0, h0), pa0, od, 0, 0, 0);
;     od = __builtin_amdgcn_mfma_f32_32x32x16_bf16(AT_PK(l1, h1), pa1, od, 0, 0, 0);
;     od = __builtin_amdgcn_mfma_f32_32x32x16_bf16(AT_PK(l2, h2), pa2, od, 0, 0, 0);
;     od = __builtin_amdgcn_mfma_f32_32x32x16_bf16(AT_PK(l3, h3), pa3, od, 0, 0, 0);
;     ...
; }
; DI void pv_all_sm(f32x16* o, int vb, bf16x8 pa0, bf16x8 pa1, bf16x8 pa2, bf16x8 pa3, f32x16& p0, f32x16& p1, float& m_ref, f32x16& negm, float& alpha) {
;     pv_one<0>(o[0], vb, pa0, pa1, pa2, pa3);
;     float pmax = p0[0];
; #pragma unroll
;     for (int r = 1; r < 16; ++r) pmax = fmaxf(pmax, p0[r]);
.LBB4_796:
	v_exp_f32_e32 v182, v128
	v_exp_f32_e32 v234, v129
	v_exp_f32_e32 v235, v130
	v_exp_f32_e32 v236, v131
	v_exp_f32_e32 v237, v132
	v_exp_f32_e32 v238, v133
	v_exp_f32_e32 v239, v134
	v_exp_f32_e32 v240, v135
	v_exp_f32_e32 v241, v136
	v_exp_f32_e32 v242, v137
	v_exp_f32_e32 v243, v138
	v_exp_f32_e32 v244, v139
	v_exp_f32_e32 v245, v140
	v_exp_f32_e32 v246, v141
	v_exp_f32_e32 v247, v142
	v_exp_f32_e32 v248, v143
	v_add_u32_e32 v101, s65, v208
	v_add_u32_e32 v102, s65, v209
	v_add_u32_e32 v103, s65, v210
	ds_read_b128 v[172:175], v101 offset:49152
	ds_read_b128 v[176:179], v101 offset:53248
	ds_read_b128 v[218:221], v102 offset:49152
	ds_read_b128 v[222:225], v102 offset:53248
	ds_read_b128 v[226:229], v103 offset:49152
	ds_read_b128 v[230:233], v103 offset:53248
	v_exp_f32_e32 v112, v112
	v_exp_f32_e32 v113, v113
	v_exp_f32_e32 v114, v114
	s_waitcnt lgkmcnt(7)
	v_mfma_f32_32x32x16_bf16 v[128:143], v[96:99], v[156:159], v[80:95]
	v_exp_f32_e32 v115, v115
	v_exp_f32_e32 v116, v116
	v_exp_f32_e32 v117, v117
	v_exp_f32_e32 v118, v118
	v_exp_f32_e32 v119, v119
	s_waitcnt lgkmcnt(6)
	v_mfma_f32_32x32x16_bf16 v[96:111], v[168:171], v[156:159], v[80:95]
	v_exp_f32_e32 v168, v120
	v_add_f32_e32 v120, 0, v182
	v_add_f32_e32 v120, v234, v120
	v_add_f32_e32 v120, v235, v120
	v_add_f32_e32 v120, v236, v120
	v_add_f32_e32 v120, v237, v120
	v_add_f32_e32 v120, v238, v120
	v_add_f32_e32 v120, v239, v120
	v_add_f32_e32 v120, v240, v120
	v_add_f32_e32 v120, v241, v120
	v_add_f32_e32 v120, v242, v120
	s_waitcnt lgkmcnt(5)
	v_mfma_f32_32x32x16_bf16 v[128:143], v[172:175], v[152:155], v[128:143]
	v_add_f32_e32 v120, v243, v120
	v_add_f32_e32 v120, v244, v120
	v_add_f32_e32 v120, v245, v120
	v_add_f32_e32 v120, v246, v120
	v_add_f32_e32 v120, v247, v120
	v_add_f32_e32 v120, v248, v120
	v_add_f32_e32 v120, v112, v120
	s_waitcnt lgkmcnt(4)
	v_mfma_f32_32x32x16_bf16 v[96:111], v[176:179], v[152:155], v[96:111]
	v_add_f32_e32 v120, v113, v120
	v_add_f32_e32 v120, v114, v120
	v_add_f32_e32 v120, v115, v120
	v_add_f32_e32 v120, v116, v120
	v_exp_f32_e32 v169, v121
	v_add_f32_e32 v120, v117, v120
	v_exp_f32_e32 v170, v122
	s_waitcnt lgkmcnt(3)
	v_mfma_f32_32x32x16_bf16 v[128:143], v[218:221], v[148:151], v[128:143]
	v_add_f32_e32 v120, v118, v120
	v_exp_f32_e32 v171, v123
	v_add_f32_e32 v120, v119, v120
	v_exp_f32_e32 v172, v124
	v_exp_f32_e32 v173, v125
	s_waitcnt lgkmcnt(2)
	v_mfma_f32_32x32x16_bf16 v[96:111], v[222:225], v[148:151], v[96:111]
	v_exp_f32_e32 v174, v126
	v_exp_f32_e32 v175, v127
	v_add_f32_e32 v120, v174, v120
	s_waitcnt lgkmcnt(1)
	v_mfma_f32_32x32x16_bf16 v[128:143], v[226:229], v[144:147], v[128:143]
	v_add_f32_e32 v217, v175, v120
	v_cvt_pk_bf16_f32 v120, v182, v234
	v_cvt_pk_bf16_f32 v121, v235, v236
	v_cvt_pk_bf16_f32 v122, v237, v238
	v_cvt_pk_bf16_f32 v123, v239, v240
	v_cvt_pk_bf16_f32 v124, v241, v242
	s_waitcnt lgkmcnt(0)
	v_mfma_f32_32x32x16_bf16 v[96:111], v[230:233], v[144:147], v[96:111]
	v_cvt_pk_bf16_f32 v125, v243, v244
	v_cvt_pk_bf16_f32 v126, v245, v246
	v_cvt_pk_bf16_f32 v127, v247, v248
	v_cvt_pk_bf16_f32 v112, v112, v113
	v_cvt_pk_bf16_f32 v113, v114, v115
	v_cvt_pk_bf16_f32 v114, v116, v117
	v_cvt_pk_bf16_f32 v115, v118, v119
	s_add_u32 s24, s34, 0x2380c000
	s_addc_u32 s25, s35, 0
	s_add_u32 s34, s34, 0x2380e000
	s_addc_u32 s35, s35, 0
	s_add_u32 s66, s37, 0x21886000
	s_addc_u32 s67, s64, 0
	s_lshl_b32 s92, s29, 14
	s_add_i32 s92, s92, s94
	s_mov_b32 m0, s92
	s_lshl_b32 s96, s29, 13
	global_load_lds_dwordx4 v249, s[24:25]
	s_addk_i32 s92, 0x400
	s_mov_b32 m0, s92
	s_add_i32 s96, s96, s95
	global_load_lds_dwordx4 v250, s[24:25]
	s_nop 0
	s_mov_b32 m0, s96
	s_nop 0
	global_load_lds_dwordx4 v251, s[66:67]
	s_nop 0
	s_and_b64 vcc, exec, s[2:3]
	s_cbranch_vccnz .LBB4_798
	s_mov_b64 s[2:3], s[8:9]
	global_store_dwordx2 v193, v[184:185], s[2:3] nt
.LBB4_798:
	v_lshl_add_u32 v219, s30, 14, v253
	ds_read_b64_tr_b16 v[220:221], v219 offset:0
	ds_read_b64_tr_b16 v[222:223], v219 offset:0x100
	ds_read_b64_tr_b16 v[224:225], v219 offset:0x1000
	ds_read_b64_tr_b16 v[226:227], v219 offset:0x1100
	ds_read_b64_tr_b16 v[228:229], v219 offset:0x2000
	ds_read_b64_tr_b16 v[230:231], v219 offset:0x2100
	ds_read_b64_tr_b16 v[232:233], v219 offset:0x3000
	ds_read_b64_tr_b16 v[234:235], v219 offset:0x3100
	s_waitcnt lgkmcnt(0)
	v_mfma_f32_32x32x16_bf16 v[48:63], v[220:223], v[120:123], v[48:63]
	v_max_f32_e32 v182, v128, v129
	ds_read_b64_tr_b16 v[220:221], v219 offset:0x200
	ds_read_b64_tr_b16 v[222:223], v219 offset:0x300
	v_max3_f32 v182, v182, v130, v131
	v_max3_f32 v182, v182, v132, v133
	v_mfma_f32_32x32x16_bf16 v[48:63], v[224:227], v[124:127], v[48:63]
	ds_read_b64_tr_b16 v[224:225], v219 offset:0x1200
	ds_read_b64_tr_b16 v[226:227], v219 offset:0x1300
	v_max3_f32 v182, v182, v134, v135
	v_max3_f32 v182, v182, v136, v137
	v_max3_f32 v182, v182, v138, v139
	v_max3_f32 v182, v182, v140, v141
	v_max3_f32 v182, v182, v142, v143
	v_mfma_f32_32x32x16_bf16 v[48:63], v[228:231], v[112:115], v[48:63]
	v_cvt_pk_bf16_f32 v116, v168, v169
	v_cvt_pk_bf16_f32 v117, v170, v171
	v_cvt_pk_bf16_f32 v118, v172, v173
	v_cvt_pk_bf16_f32 v119, v174, v175
	v_add_f32_e32 v254, v168, v169
	v_add_f32_e32 v254, v170, v254
	ds_read_b64_tr_b16 v[228:229], v219 offset:0x2200
	ds_read_b64_tr_b16 v[230:231], v219 offset:0x2300
	ds_read_b64_tr_b16 v[236:237], v219 offset:0x3200
	ds_read_b64_tr_b16 v[238:239], v219 offset:0x3300
	v_mfma_f32_32x32x16_bf16 v[48:63], v[232:235], v[116:119], v[48:63]
	v_add_f32_e32 v254, v171, v254
	v_add_f32_e32 v254, v172, v254
	s_waitcnt lgkmcnt(0)
	v_mfma_f32_32x32x16_bf16 v[32:47], v[220:223], v[120:123], v[32:47]
	v_max3_f32 v182, v182, v96, v97
	v_max3_f32 v182, v182, v98, v99
	ds_read_b64_tr_b16 v[222:223], v219 offset:0x400
	v_max3_f32 v182, v182, v100, v101
	v_max3_f32 v182, v182, v102, v103
	v_max3_f32 v182, v182, v104, v105
	v_max3_f32 v182, v182, v106, v107
	v_mfma_f32_32x32x16_bf16 v[32:47], v[224:227], v[124:127], v[32:47]
	ds_read_b64_tr_b16 v[224:225], v219 offset:0x500
	ds_read_b64_tr_b16 v[226:227], v219 offset:0x1400
	v_max3_f32 v182, v182, v108, v109
	v_max3_f32 v182, v182, v110, v111
	v_mov_b32_e32 v220, v182
	s_nop 1
	v_permlane32_swap_b32_e32 v182, v220
	v_mfma_f32_32x32x16_bf16 v[32:47], v[228:231], v[112:115], v[32:47]
	ds_read_b64_tr_b16 v[228:229], v219 offset:0x1500
	ds_read_b64_tr_b16 v[230:231], v219 offset:0x2400
	ds_read_b64_tr_b16 v[232:233], v219 offset:0x2500
	ds_read_b64_tr_b16 v[240:241], v219 offset:0x3400
	ds_read_b64_tr_b16 v[242:243], v219 offset:0x3500
	v_mfma_f32_32x32x16_bf16 v[32:47], v[236:239], v[116:119], v[32:47]
	s_waitcnt lgkmcnt(0)
	v_max_f32_e32 v220, v182, v220
	v_mfma_f32_32x32x16_bf16 v[16:31], v[222:225], v[120:123], v[16:31]
	v_cmp_ge_f32_e32 vcc, s26, v220
	s_cmp_eq_u64 vcc, exec
	v_mov_b32_e32 v182, 1.0
	v_mfma_f32_32x32x16_bf16 v[16:31], v[226:229], v[124:127], v[16:31]
	v_mfma_f32_32x32x16_bf16 v[16:31], v[230:233], v[112:115], v[16:31]
	v_mfma_f32_32x32x16_bf16 v[16:31], v[240:243], v[116:119], v[16:31]
	s_cbranch_scc0 .LBB4_811

; DI void finishSM(f32x16& p0, f32x16& p1, float alpha, float& l_reg, bf16x8& pa0, bf16x8& pa1, bf16x8& pa2, bf16x8& pa3) {
; #pragma unroll
;     for (int r = 0; r < 16; ++r) p1[r] = __builtin_amdgcn_exp2f(p1[r]);
;     float ps = 0;
; #pragma unroll
;     for (int r = 0; r < 16; ++r) ps += p0[r];
; #pragma unroll
;     for (int r = 0; r < 16; ++r) ps += p1[r];
;     { auto rr = __builtin_amdgcn_permlane32_swap(__float_as_uint(ps), __float_as_uint(ps), false, false); ps = __uint_as_float(rr[0]) + __uint_as_float(rr[1]); }
;     l_reg = l_reg * alpha + ps;
;     ...
;     AT_PK4(p0, 0, pa0); AT_PK4(p0, 8, pa1); AT_PK4(p1, 0, pa2); AT_PK4(p1, 8, pa3);
;     ...
; }
; DI void qkt(f32x16& p0, f32x16& p1, const char* Ks, const bf16x8* qr, const f32x16& negm, int r32, int hi) {
; #pragma unroll
;     for (int d0 = 0; d0 < 4; ++d0) { const int cb = (d0 * 16 + hi * 8) * 2;
;         const bf16x8 b0 = *reinterpret_cast<const bf16x8*>(Ks + AT_KSWZ(r32, cb));
;         const bf16x8 b1 = *reinterpret_cast<const bf16x8*>(Ks + AT_KSWZ(32 + r32, cb));
;         p0 = __builtin_amdgcn_mfma_f32_32x32x16_bf16(b0, qr[d0], d0 == 0 ? negm : p0, 0, 0, 0);
;         p1 = __builtin_amdgcn_mfma_f32_32x32x16_bf16(b1, qr[d0], d0 == 0 ? negm : p1, 0, 0, 0); }
; }
; template <int D0> DI void pv_one(f32x16& od, int vb, bf16x8 pa0, bf16x8 pa1, bf16x8 pa2, bf16x8 pa3) {
;     const s16x4 l0 = tr_read<v_rd_off(D0, 0, 0)>(vb), h0 = tr_read<v_rd_off(D0, 0, 1)>(vb), l1 = tr_read<v_rd_off(D0, 1, 0)>(vb), h1 = tr_read<v_rd_off(D0, 1, 1)>(vb);
;     const s16x4 l2 = tr_read<v_rd_off(D0, 2, 0)>(vb), h2 = tr_read<v_rd_off(D0, 2, 1)>(vb), l3 = tr_read<v_rd_off(D0, 3, 0)>(vb), h3 = tr_read<v_rd_off(D0, 3, 1)>(vb);
;     asm volatile("s_waitcnt lgkmcnt(0)" ::: "memory"); AT_SBAR();
;     ...
;     od = __builtin_amdgcn_mfma_f32_32x32x16_bf16(AT_PK(l0, h0), pa0, od, 0, 0, 0);
;     od = __builtin_amdgcn_mfma_f32_32x32x16_bf16(AT_PK(l1, h1), pa1, od, 0, 0, 0);
;     od = __builtin_amdgcn_mfma_f32_32x32x16_bf16(AT_PK(l2, h2), pa2, od, 0, 0, 0);
;     od = __builtin_amdgcn_mfma_f32_32x32x16_bf16(AT_PK(l3, h3), pa3, od, 0, 0, 0);
;     ...
; }
; DI void pv_all_sm(f32x16* o, int vb, bf16x8 pa0, bf16x8 pa1, bf16x8 pa2, bf16x8 pa3, f32x16& p0, f32x16& p1, float& m_ref, f32x16& negm, float& alpha) {
;     pv_one<0>(o[0], vb, pa0, pa1, pa2, pa3);
;     float pmax = p0[0];
; #pragma unroll
;     for (int r = 1; r < 16; ++r) pmax = fmaxf(pmax, p0[r]);
.LBB4_849:
	s_lshl_b32 s26, s64, 13
	s_add_i32 s26, s26, 0
	v_add_u32_e32 v72, s26, v204
	v_add_u32_e32 v112, s26, v205
	v_add_u32_e32 v180, s26, v206
	s_waitcnt lgkmcnt(1)
	v_mfma_f32_32x32x16_bf16 v[128:143], v[64:67], v[156:159], v[80:95]
	ds_read_b128 v[64:67], v72 offset:49152
	ds_read_b128 v[72:75], v72 offset:53248
	ds_read_b128 v[76:79], v112 offset:49152
	ds_read_b128 v[220:223], v112 offset:53248
	v_exp_f32_e32 v182, v97
	v_exp_f32_e32 v213, v98
	v_exp_f32_e32 v214, v99
	v_exp_f32_e32 v219, v100
	v_exp_f32_e32 v228, v101
	s_waitcnt lgkmcnt(4)
	v_mfma_f32_32x32x16_bf16 v[112:127], v[68:71], v[156:159], v[80:95]
	ds_read_b128 v[68:71], v180 offset:49152
	ds_read_b128 v[224:227], v180 offset:53248
	v_exp_f32_e32 v180, v96
	v_cvt_pk_bf16_f32 v96, v216, v218
	v_cvt_pk_bf16_f32 v97, v179, v217
	v_cvt_pk_bf16_f32 v98, v177, v215
	v_cvt_pk_bf16_f32 v99, v176, v178
	s_waitcnt lgkmcnt(4)
	v_mfma_f32_32x32x16_bf16 v[112:127], v[72:75], v[152:155], v[112:127]
	v_add_f32_e32 v75, 0, v216
	v_add_f32_e32 v75, v218, v75
	v_add_f32_e32 v75, v217, v75
	v_add_f32_e32 v75, v215, v75
	v_add_f32_e32 v75, v176, v75
	v_mfma_f32_32x32x16_bf16 v[128:143], v[64:67], v[152:155], v[128:143]
	v_add_f32_e32 v75, v172, v75
	s_waitcnt lgkmcnt(3)
	v_mfma_f32_32x32x16_bf16 v[128:143], v[76:79], v[148:151], v[128:143]
	v_add_f32_e32 v75, v180, v75
	v_add_f32_e32 v75, v182, v75
	v_exp_f32_e32 v64, v102
	v_exp_f32_e32 v65, v103
	v_exp_f32_e32 v66, v104
	s_waitcnt lgkmcnt(2)
	v_mfma_f32_32x32x16_bf16 v[112:127], v[220:223], v[148:151], v[112:127]
	v_exp_f32_e32 v67, v105
	v_exp_f32_e32 v105, v106
	v_exp_f32_e32 v106, v107
	v_exp_f32_e32 v107, v108
	v_exp_f32_e32 v72, v109
	v_exp_f32_e32 v73, v110
	v_exp_f32_e32 v74, v111
	s_waitcnt lgkmcnt(1)
	v_mfma_f32_32x32x16_bf16 v[128:143], v[68:71], v[144:147], v[128:143]
	v_add_f32_e32 v68, v213, v75
	v_add_f32_e32 v68, v214, v68
	v_add_f32_e32 v68, v219, v68
	v_add_f32_e32 v68, v228, v68
	v_add_f32_e32 v68, v64, v68
	v_add_f32_e32 v68, v65, v68
	v_add_f32_e32 v68, v66, v68
	v_add_f32_e32 v68, v67, v68
	s_waitcnt lgkmcnt(0)
	v_mfma_f32_32x32x16_bf16 v[112:127], v[224:227], v[144:147], v[112:127]
	v_add_f32_e32 v68, v105, v68
	v_add_f32_e32 v68, v106, v68
	v_add_f32_e32 v68, v107, v68
	v_add_f32_e32 v68, v72, v68
	v_add_f32_e32 v68, v73, v68
	v_add_f32_e32 v211, v74, v68
	v_cvt_pk_bf16_f32 v100, v180, v182
	v_cvt_pk_bf16_f32 v101, v213, v214
	v_cvt_pk_bf16_f32 v102, v219, v228
	v_cvt_pk_bf16_f32 v103, v64, v65
	v_cvt_pk_bf16_f32 v104, v66, v67
	v_cvt_pk_bf16_f32 v105, v105, v106
	v_cvt_pk_bf16_f32 v106, v107, v72
	v_cvt_pk_bf16_f32 v107, v73, v74
	s_add_u32 s66, s46, s28
	s_addc_u32 s67, s47, s29
	s_add_u32 s34, s66, 0x23808000
	s_addc_u32 s35, s67, 0
	s_add_u32 s76, s66, 0x2380a000
	s_addc_u32 s77, s67, 0
	s_add_u32 s74, s46, s24
	s_addc_u32 s75, s47, s25
	s_add_u32 s78, s74, 0x21804000
	s_addc_u32 s79, s75, 0
	s_lshl_b32 s92, s57, 14
	s_add_i32 s92, s92, s94
	s_mov_b32 m0, s92
	s_lshl_b32 s96, s57, 13
	global_load_lds_dwordx4 v249, s[34:35]
	s_addk_i32 s92, 0x400
	s_mov_b32 m0, s92
	s_add_i32 s96, s96, s95
	global_load_lds_dwordx4 v250, s[34:35]
	s_nop 0
	s_mov_b32 m0, s96
	s_nop 0
	global_load_lds_dwordx4 v251, s[78:79]
	s_andn2_b64 vcc, exec, s[2:3]
	s_cbranch_vccnz .LBB4_851
	s_mov_b64 s[2:3], s[8:9]
	global_store_dwordx2 v188, v[184:185], s[2:3] nt
.LBB4_851:
	s_lshl_b32 s65, s63, 14
	v_add_u32_e32 v182, s65, v253
	ds_read_b64_tr_b16 v[64:65], v182 offset:0
	ds_read_b64_tr_b16 v[66:67], v182 offset:0x100
	ds_read_b64_tr_b16 v[68:69], v182 offset:0x1000
	ds_read_b64_tr_b16 v[70:71], v182 offset:0x1100
	ds_read_b64_tr_b16 v[72:73], v182 offset:0x2000
	ds_read_b64_tr_b16 v[74:75], v182 offset:0x2100
	ds_read_b64_tr_b16 v[76:77], v182 offset:0x3000
	ds_read_b64_tr_b16 v[78:79], v182 offset:0x3100
	s_waitcnt lgkmcnt(0)
	v_mfma_f32_32x32x16_bf16 v[32:47], v[64:67], v[96:99], v[32:47]
	v_cvt_pk_bf16_f32 v108, v173, v175
	v_cvt_pk_bf16_f32 v109, v171, v174
	v_cvt_pk_bf16_f32 v110, v169, v172
	v_cvt_pk_bf16_f32 v111, v168, v170
	v_max_f32_e32 v64, v128, v129
	v_max3_f32 v64, v64, v130, v131
	v_max3_f32 v64, v64, v132, v133
	v_max3_f32 v64, v64, v134, v135
	v_max3_f32 v64, v64, v136, v137
	v_mfma_f32_32x32x16_bf16 v[32:47], v[68:71], v[108:111], v[32:47]
	v_max3_f32 v64, v64, v138, v139
	v_max3_f32 v66, v64, v140, v141
	ds_read_b64_tr_b16 v[64:65], v182 offset:0x200
	v_max3_f32 v180, v66, v142, v143
	ds_read_b64_tr_b16 v[66:67], v182 offset:0x300
	ds_read_b64_tr_b16 v[68:69], v182 offset:0x1200
	ds_read_b64_tr_b16 v[70:71], v182 offset:0x1300
	v_mfma_f32_32x32x16_bf16 v[32:47], v[72:75], v[100:103], v[32:47]
	v_add_f32_e32 v254, v179, v177
	v_add_f32_e32 v254, v178, v254
	ds_read_b64_tr_b16 v[72:73], v182 offset:0x2200
	ds_read_b64_tr_b16 v[74:75], v182 offset:0x2300
	ds_read_b64_tr_b16 v[214:215], v182 offset:0x3200
	ds_read_b64_tr_b16 v[216:217], v182 offset:0x3300
	v_mfma_f32_32x32x16_bf16 v[32:47], v[76:79], v[104:107], v[32:47]
	v_add_f32_e32 v254, v173, v254
	v_add_f32_e32 v254, v175, v254
	s_waitcnt lgkmcnt(0)
	v_mfma_f32_32x32x16_bf16 v[48:63], v[64:67], v[96:99], v[48:63]
	v_add_f32_e32 v254, v171, v254
	v_add_f32_e32 v254, v174, v254
	v_max3_f32 v76, v180, v112, v113
	v_max3_f32 v64, v76, v114, v115
	ds_read_b64_tr_b16 v[66:67], v182 offset:0x400
	v_max3_f32 v64, v64, v116, v117
	v_max3_f32 v64, v64, v118, v119
	v_max3_f32 v64, v64, v120, v121
	v_max3_f32 v64, v64, v122, v123
	v_mfma_f32_32x32x16_bf16 v[48:63], v[68:71], v[108:111], v[48:63]
	v_add_f32_e32 v254, v169, v254
	v_add_f32_e32 v254, v168, v254
	ds_read_b64_tr_b16 v[68:69], v182 offset:0x500
	ds_read_b64_tr_b16 v[70:71], v182 offset:0x1400
	v_max3_f32 v64, v64, v124, v125
	v_max3_f32 v64, v64, v126, v127
	v_mov_b32_e32 v65, v64
	s_nop 1
	v_permlane32_swap_b32_e32 v64, v65
	v_mfma_f32_32x32x16_bf16 v[48:63], v[72:75], v[100:103], v[48:63]
	ds_read_b64_tr_b16 v[72:73], v182 offset:0x1500
	ds_read_b64_tr_b16 v[74:75], v182 offset:0x2400
	ds_read_b64_tr_b16 v[76:77], v182 offset:0x2500
	ds_read_b64_tr_b16 v[218:219], v182 offset:0x3400
	ds_read_b64_tr_b16 v[220:221], v182 offset:0x3500
	v_mfma_f32_32x32x16_bf16 v[48:63], v[214:217], v[104:107], v[48:63]
	s_waitcnt lgkmcnt(0)
	v_max_f32_e32 v64, v64, v65
	v_mfma_f32_32x32x16_bf16 v[16:31], v[66:69], v[96:99], v[16:31]
	v_cmp_ge_f32_e32 vcc, s15, v64
	s_cmp_eq_u64 vcc, exec
	v_mfma_f32_32x32x16_bf16 v[16:31], v[70:73], v[108:111], v[16:31]
	v_mfma_f32_32x32x16_bf16 v[16:31], v[74:77], v[100:103], v[16:31]
	v_mfma_f32_32x32x16_bf16 v[16:31], v[218:221], v[104:107], v[16:31]
	s_cbranch_scc0 .LBB4_884
	v_mov_b32_e32 v180, 1.0

; DI void finishSM(f32x16& p0, f32x16& p1, float alpha, float& l_reg, bf16x8& pa0, bf16x8& pa1, bf16x8& pa2, bf16x8& pa3) {
; #pragma unroll
;     for (int r = 0; r < 16; ++r) p1[r] = __builtin_amdgcn_exp2f(p1[r]);
;     float ps = 0;
; #pragma unroll
;     for (int r = 0; r < 16; ++r) ps += p0[r];
; #pragma unroll
;     for (int r = 0; r < 16; ++r) ps += p1[r];
;     { auto rr = __builtin_amdgcn_permlane32_swap(__float_as_uint(ps), __float_as_uint(ps), false, false); ps = __uint_as_float(rr[0]) + __uint_as_float(rr[1]); }
;     l_reg = l_reg * alpha + ps;
;     ...
;     AT_PK4(p0, 0, pa0); AT_PK4(p0, 8, pa1); AT_PK4(p1, 0, pa2); AT_PK4(p1, 8, pa3);
;     ...
; }
; DI void qkt(f32x16& p0, f32x16& p1, const char* Ks, const bf16x8* qr, const f32x16& negm, int r32, int hi) {
; #pragma unroll
;     for (int d0 = 0; d0 < 4; ++d0) { const int cb = (d0 * 16 + hi * 8) * 2;
;         const bf16x8 b0 = *reinterpret_cast<const bf16x8*>(Ks + AT_KSWZ(r32, cb));
;         const bf16x8 b1 = *reinterpret_cast<const bf16x8*>(Ks + AT_KSWZ(32 + r32, cb));
;         p0 = __builtin_amdgcn_mfma_f32_32x32x16_bf16(b0, qr[d0], d0 == 0 ? negm : p0, 0, 0, 0);
;         p1 = __builtin_amdgcn_mfma_f32_32x32x16_bf16(b1, qr[d0], d0 == 0 ? negm : p1, 0, 0, 0); }
; }
; template <int D0> DI void pv_one(f32x16& od, int vb, bf16x8 pa0, bf16x8 pa1, bf16x8 pa2, bf16x8 pa3) {
;     const s16x4 l0 = tr_read<v_rd_off(D0, 0, 0)>(vb), h0 = tr_read<v_rd_off(D0, 0, 1)>(vb), l1 = tr_read<v_rd_off(D0, 1, 0)>(vb), h1 = tr_read<v_rd_off(D0, 1, 1)>(vb);
;     const s16x4 l2 = tr_read<v_rd_off(D0, 2, 0)>(vb), h2 = tr_read<v_rd_off(D0, 2, 1)>(vb), l3 = tr_read<v_rd_off(D0, 3, 0)>(vb), h3 = tr_read<v_rd_off(D0, 3, 1)>(vb);
;     asm volatile("s_waitcnt lgkmcnt(0)" ::: "memory"); AT_SBAR();
;     ...
;     od = __builtin_amdgcn_mfma_f32_32x32x16_bf16(AT_PK(l0, h0), pa0, od, 0, 0, 0);
;     od = __builtin_amdgcn_mfma_f32_32x32x16_bf16(AT_PK(l1, h1), pa1, od, 0, 0, 0);
;     od = __builtin_amdgcn_mfma_f32_32x32x16_bf16(AT_PK(l2, h2), pa2, od, 0, 0, 0);
;     od = __builtin_amdgcn_mfma_f32_32x32x16_bf16(AT_PK(l3, h3), pa3, od, 0, 0, 0);
;     ...
; }
; DI void pv_all_sm(f32x16* o, int vb, bf16x8 pa0, bf16x8 pa1, bf16x8 pa2, bf16x8 pa3, f32x16& p0, f32x16& p1, float& m_ref, f32x16& negm, float& alpha) {
;     pv_one<0>(o[0], vb, pa0, pa1, pa2, pa3);
;     float pmax = p0[0];
; #pragma unroll
;     for (int r = 1; r < 16; ++r) pmax = fmaxf(pmax, p0[r]);
.LBB4_870:
	v_exp_f32_e32 v182, v128
	v_exp_f32_e32 v230, v129
	v_exp_f32_e32 v231, v130
	v_exp_f32_e32 v232, v131
	v_exp_f32_e32 v233, v132
	v_exp_f32_e32 v234, v133
	v_exp_f32_e32 v235, v134
	v_exp_f32_e32 v236, v135
	v_exp_f32_e32 v237, v136
	v_exp_f32_e32 v238, v137
	v_exp_f32_e32 v239, v138
	v_exp_f32_e32 v240, v139
	v_exp_f32_e32 v241, v140
	v_exp_f32_e32 v242, v141
	v_exp_f32_e32 v243, v142
	v_exp_f32_e32 v244, v143
	v_add_u32_e32 v101, s76, v204
	v_add_u32_e32 v102, s76, v205
	v_add_u32_e32 v103, s76, v206
	ds_read_b128 v[172:175], v101 offset:49152
	ds_read_b128 v[176:179], v101 offset:53248
	ds_read_b128 v[214:217], v102 offset:49152
	ds_read_b128 v[218:221], v102 offset:53248
	ds_read_b128 v[222:225], v103 offset:49152
	ds_read_b128 v[226:229], v103 offset:53248
	v_exp_f32_e32 v112, v112
	v_exp_f32_e32 v113, v113
	v_exp_f32_e32 v114, v114
	s_waitcnt lgkmcnt(7)
	v_mfma_f32_32x32x16_bf16 v[128:143], v[96:99], v[156:159], v[80:95]
	v_exp_f32_e32 v115, v115
	v_exp_f32_e32 v116, v116
	v_exp_f32_e32 v117, v117
	v_exp_f32_e32 v118, v118
	v_exp_f32_e32 v119, v119
	s_waitcnt lgkmcnt(6)
	v_mfma_f32_32x32x16_bf16 v[96:111], v[168:171], v[156:159], v[80:95]
	v_exp_f32_e32 v168, v120
	v_add_f32_e32 v120, 0, v182
	v_add_f32_e32 v120, v230, v120
	v_add_f32_e32 v120, v231, v120
	v_add_f32_e32 v120, v232, v120
	v_add_f32_e32 v120, v233, v120
	v_add_f32_e32 v120, v234, v120
	v_add_f32_e32 v120, v235, v120
	v_add_f32_e32 v120, v236, v120
	v_add_f32_e32 v120, v237, v120
	v_add_f32_e32 v120, v238, v120
	s_waitcnt lgkmcnt(5)
	v_mfma_f32_32x32x16_bf16 v[128:143], v[172:175], v[152:155], v[128:143]
	v_add_f32_e32 v120, v239, v120
	v_add_f32_e32 v120, v240, v120
	v_add_f32_e32 v120, v241, v120
	v_add_f32_e32 v120, v242, v120
	v_add_f32_e32 v120, v243, v120
	v_add_f32_e32 v120, v244, v120
	v_add_f32_e32 v120, v112, v120
	s_waitcnt lgkmcnt(4)
	v_mfma_f32_32x32x16_bf16 v[96:111], v[176:179], v[152:155], v[96:111]
	v_add_f32_e32 v120, v113, v120
	v_add_f32_e32 v120, v114, v120
	v_add_f32_e32 v120, v115, v120
	v_add_f32_e32 v120, v116, v120
	v_exp_f32_e32 v169, v121
	v_add_f32_e32 v120, v117, v120
	v_exp_f32_e32 v170, v122
	s_waitcnt lgkmcnt(3)
	v_mfma_f32_32x32x16_bf16 v[128:143], v[214:217], v[148:151], v[128:143]
	v_add_f32_e32 v120, v118, v120
	v_exp_f32_e32 v171, v123
	v_add_f32_e32 v120, v119, v120
	v_exp_f32_e32 v172, v124
	v_exp_f32_e32 v173, v125
	s_waitcnt lgkmcnt(2)
	v_mfma_f32_32x32x16_bf16 v[96:111], v[218:221], v[148:151], v[96:111]
	v_exp_f32_e32 v174, v126
	v_exp_f32_e32 v175, v127
	v_add_f32_e32 v120, v174, v120
	s_waitcnt lgkmcnt(1)
	v_mfma_f32_32x32x16_bf16 v[128:143], v[222:225], v[144:147], v[128:143]
	v_add_f32_e32 v213, v175, v120
	v_cvt_pk_bf16_f32 v120, v182, v230
	v_cvt_pk_bf16_f32 v121, v231, v232
	v_cvt_pk_bf16_f32 v122, v233, v234
	v_cvt_pk_bf16_f32 v123, v235, v236
	v_cvt_pk_bf16_f32 v124, v237, v238
	s_waitcnt lgkmcnt(0)
	v_mfma_f32_32x32x16_bf16 v[96:111], v[226:229], v[144:147], v[96:111]
	v_cvt_pk_bf16_f32 v125, v239, v240
	v_cvt_pk_bf16_f32 v126, v241, v242
	v_cvt_pk_bf16_f32 v127, v243, v244
	v_cvt_pk_bf16_f32 v112, v112, v113
	v_cvt_pk_bf16_f32 v113, v114, v115
	v_cvt_pk_bf16_f32 v114, v116, v117
	v_cvt_pk_bf16_f32 v115, v118, v119
	s_add_u32 s34, s66, 0x2380c000
	s_addc_u32 s35, s67, 0
	s_add_u32 s66, s66, 0x2380e000
	s_addc_u32 s67, s67, 0
	s_add_u32 s74, s74, 0x21806000
	s_addc_u32 s75, s75, 0
	s_lshl_b32 s92, s63, 14
	s_add_i32 s92, s92, s94
	s_mov_b32 m0, s92
	s_lshl_b32 s96, s63, 13
	global_load_lds_dwordx4 v249, s[34:35]
	s_addk_i32 s92, 0x400
	s_mov_b32 m0, s92
	s_add_i32 s96, s96, s95
	global_load_lds_dwordx4 v250, s[34:35]
	s_nop 0
	s_mov_b32 m0, s96
	s_nop 0
	global_load_lds_dwordx4 v251, s[74:75]
	s_nop 0
	s_and_b64 vcc, exec, s[2:3]
	s_cbranch_vccnz .LBB4_872
	s_mov_b64 s[2:3], s[8:9]
	global_store_dwordx2 v188, v[184:185], s[2:3] nt
.LBB4_872:
	v_lshl_add_u32 v215, s64, 14, v253
	ds_read_b64_tr_b16 v[216:217], v215 offset:0
	ds_read_b64_tr_b16 v[218:219], v215 offset:0x100
	ds_read_b64_tr_b16 v[220:221], v215 offset:0x1000
	ds_read_b64_tr_b16 v[222:223], v215 offset:0x1100
	ds_read_b64_tr_b16 v[224:225], v215 offset:0x2000
	ds_read_b64_tr_b16 v[226:227], v215 offset:0x2100
	ds_read_b64_tr_b16 v[228:229], v215 offset:0x3000
	ds_read_b64_tr_b16 v[230:231], v215 offset:0x3100
	s_waitcnt lgkmcnt(0)
	v_mfma_f32_32x32x16_bf16 v[32:47], v[216:219], v[120:123], v[32:47]
	v_max_f32_e32 v182, v128, v129
	ds_read_b64_tr_b16 v[216:217], v215 offset:0x200
	ds_read_b64_tr_b16 v[218:219], v215 offset:0x300
	v_max3_f32 v182, v182, v130, v131
	v_max3_f32 v182, v182, v132, v133
	v_mfma_f32_32x32x16_bf16 v[32:47], v[220:223], v[124:127], v[32:47]
	ds_read_b64_tr_b16 v[220:221], v215 offset:0x1200
	ds_read_b64_tr_b16 v[222:223], v215 offset:0x1300
	v_max3_f32 v182, v182, v134, v135
	v_max3_f32 v182, v182, v136, v137
	v_max3_f32 v182, v182, v138, v139
	v_max3_f32 v182, v182, v140, v141
	v_max3_f32 v182, v182, v142, v143
	v_mfma_f32_32x32x16_bf16 v[32:47], v[224:227], v[112:115], v[32:47]
	v_cvt_pk_bf16_f32 v116, v168, v169
	v_cvt_pk_bf16_f32 v117, v170, v171
	v_cvt_pk_bf16_f32 v118, v172, v173
	v_cvt_pk_bf16_f32 v119, v174, v175
	v_add_f32_e32 v254, v168, v169
	v_add_f32_e32 v254, v170, v254
	ds_read_b64_tr_b16 v[224:225], v215 offset:0x2200
	ds_read_b64_tr_b16 v[226:227], v215 offset:0x2300
	ds_read_b64_tr_b16 v[232:233], v215 offset:0x3200
	ds_read_b64_tr_b16 v[234:235], v215 offset:0x3300
	v_mfma_f32_32x32x16_bf16 v[32:47], v[228:231], v[116:119], v[32:47]
	v_add_f32_e32 v254, v171, v254
	v_add_f32_e32 v254, v172, v254
	s_waitcnt lgkmcnt(0)
	v_mfma_f32_32x32x16_bf16 v[48:63], v[216:219], v[120:123], v[48:63]
	v_max3_f32 v182, v182, v96, v97
	v_max3_f32 v182, v182, v98, v99
	ds_read_b64_tr_b16 v[218:219], v215 offset:0x400
	v_max3_f32 v182, v182, v100, v101
	v_max3_f32 v182, v182, v102, v103
	v_max3_f32 v182, v182, v104, v105
	v_max3_f32 v182, v182, v106, v107
	v_mfma_f32_32x32x16_bf16 v[48:63], v[220:223], v[124:127], v[48:63]
	ds_read_b64_tr_b16 v[220:221], v215 offset:0x500
	ds_read_b64_tr_b16 v[222:223], v215 offset:0x1400
	v_max3_f32 v182, v182, v108, v109
	v_max3_f32 v182, v182, v110, v111
	v_mov_b32_e32 v216, v182
	s_nop 1
	v_permlane32_swap_b32_e32 v182, v216
	v_mfma_f32_32x32x16_bf16 v[48:63], v[224:227], v[112:115], v[48:63]
	ds_read_b64_tr_b16 v[224:225], v215 offset:0x1500
	ds_read_b64_tr_b16 v[226:227], v215 offset:0x2400
	ds_read_b64_tr_b16 v[228:229], v215 offset:0x2500
	ds_read_b64_tr_b16 v[236:237], v215 offset:0x3400
	ds_read_b64_tr_b16 v[238:239], v215 offset:0x3500
	v_mfma_f32_32x32x16_bf16 v[48:63], v[232:235], v[116:119], v[48:63]
	s_waitcnt lgkmcnt(0)
	v_max_f32_e32 v216, v182, v216
	v_mfma_f32_32x32x16_bf16 v[16:31], v[218:221], v[120:123], v[16:31]
	v_cmp_ge_f32_e32 vcc, s15, v216
	s_cmp_eq_u64 vcc, exec
	v_mov_b32_e32 v182, 1.0
	v_mfma_f32_32x32x16_bf16 v[16:31], v[222:225], v[124:127], v[16:31]
	v_mfma_f32_32x32x16_bf16 v[16:31], v[226:229], v[112:115], v[16:31]
	v_mfma_f32_32x32x16_bf16 v[16:31], v[236:239], v[116:119], v[16:31]
	s_cbranch_scc0 .LBB4_885

; DI void finishSM(f32x16& p0, f32x16& p1, float alpha, float& l_reg, bf16x8& pa0, bf16x8& pa1, bf16x8& pa2, bf16x8& pa3) {
; #pragma unroll
;     for (int r = 0; r < 16; ++r) p1[r] = __builtin_amdgcn_exp2f(p1[r]);
;     float ps = 0;
; #pragma unroll
;     for (int r = 0; r < 16; ++r) ps += p0[r];
; #pragma unroll
;     for (int r = 0; r < 16; ++r) ps += p1[r];
;     { auto rr = __builtin_amdgcn_permlane32_swap(__float_as_uint(ps), __float_as_uint(ps), false, false); ps = __uint_as_float(rr[0]) + __uint_as_float(rr[1]); }
;     l_reg = l_reg * alpha + ps;
;     ...
;     AT_PK4(p0, 0, pa0); AT_PK4(p0, 8, pa1); AT_PK4(p1, 0, pa2); AT_PK4(p1, 8, pa3);
;     ...
; }
; DI void qkt(f32x16& p0, f32x16& p1, const char* Ks, const bf16x8* qr, const f32x16& negm, int r32, int hi) {
; #pragma unroll
;     for (int d0 = 0; d0 < 4; ++d0) { const int cb = (d0 * 16 + hi * 8) * 2;
;         const bf16x8 b0 = *reinterpret_cast<const bf16x8*>(Ks + AT_KSWZ(r32, cb));
;         const bf16x8 b1 = *reinterpret_cast<const bf16x8*>(Ks + AT_KSWZ(32 + r32, cb));
;         p0 = __builtin_amdgcn_mfma_f32_32x32x16_bf16(b0, qr[d0], d0 == 0 ? negm : p0, 0, 0, 0);
;         p1 = __builtin_amdgcn_mfma_f32_32x32x16_bf16(b1, qr[d0], d0 == 0 ? negm : p1, 0, 0, 0); }
; }
.LBB4_923:
	s_lshl_b32 s18, s30, 13
	s_add_i32 s18, s18, 0
	v_add_u32_e32 v72, s18, v208
	v_add_u32_e32 v112, s18, v209
	v_add_u32_e32 v180, s18, v210
	s_waitcnt lgkmcnt(1)
	v_mfma_f32_32x32x16_bf16 v[128:143], v[64:67], v[156:159], v[80:95]
	ds_read_b128 v[64:67], v72 offset:49152
	ds_read_b128 v[72:75], v72 offset:53248
	ds_read_b128 v[76:79], v112 offset:49152
	ds_read_b128 v[224:227], v112 offset:53248
	v_exp_f32_e32 v182, v97
	v_exp_f32_e32 v217, v98
	v_exp_f32_e32 v218, v99
	v_exp_f32_e32 v223, v100
	v_exp_f32_e32 v232, v101
	s_waitcnt lgkmcnt(4)
	v_mfma_f32_32x32x16_bf16 v[112:127], v[68:71], v[156:159], v[80:95]
	ds_read_b128 v[68:71], v180 offset:49152
	ds_read_b128 v[228:231], v180 offset:53248
	v_exp_f32_e32 v180, v96
	v_cvt_pk_bf16_f32 v96, v220, v222
	v_cvt_pk_bf16_f32 v97, v179, v221
	v_cvt_pk_bf16_f32 v98, v177, v219
	v_cvt_pk_bf16_f32 v99, v176, v178
	s_waitcnt lgkmcnt(4)
	v_mfma_f32_32x32x16_bf16 v[112:127], v[72:75], v[152:155], v[112:127]
	v_add_f32_e32 v75, 0, v220
	v_add_f32_e32 v75, v222, v75
	v_add_f32_e32 v75, v221, v75
	v_add_f32_e32 v75, v219, v75
	v_add_f32_e32 v75, v176, v75
	v_mfma_f32_32x32x16_bf16 v[128:143], v[64:67], v[152:155], v[128:143]
	v_add_f32_e32 v75, v172, v75
	s_waitcnt lgkmcnt(3)
	v_mfma_f32_32x32x16_bf16 v[128:143], v[76:79], v[148:151], v[128:143]
	v_add_f32_e32 v75, v180, v75
	v_add_f32_e32 v75, v182, v75
	v_exp_f32_e32 v64, v102
	v_exp_f32_e32 v65, v103
	v_exp_f32_e32 v66, v104
	s_waitcnt lgkmcnt(2)
	v_mfma_f32_32x32x16_bf16 v[112:127], v[224:227], v[148:151], v[112:127]
	v_exp_f32_e32 v67, v105
	v_exp_f32_e32 v105, v106
	v_exp_f32_e32 v106, v107
	v_exp_f32_e32 v107, v108
	v_exp_f32_e32 v72, v109
	v_exp_f32_e32 v73, v110
	v_exp_f32_e32 v74, v111
	s_waitcnt lgkmcnt(1)
	v_mfma_f32_32x32x16_bf16 v[128:143], v[68:71], v[144:147], v[128:143]
	v_add_f32_e32 v68, v217, v75
	v_add_f32_e32 v68, v218, v68
	v_add_f32_e32 v68, v223, v68
	v_add_f32_e32 v68, v232, v68
	v_add_f32_e32 v68, v64, v68
	v_add_f32_e32 v68, v65, v68
	v_add_f32_e32 v68, v66, v68
	v_add_f32_e32 v68, v67, v68
	s_waitcnt lgkmcnt(0)
	v_mfma_f32_32x32x16_bf16 v[112:127], v[228:231], v[144:147], v[112:127]
	v_add_f32_e32 v68, v105, v68
	v_add_f32_e32 v68, v106, v68
	v_add_f32_e32 v68, v107, v68
	v_add_f32_e32 v68, v72, v68
	v_add_f32_e32 v68, v73, v68
	v_add_f32_e32 v215, v74, v68
	v_cvt_pk_bf16_f32 v100, v180, v182
	v_cvt_pk_bf16_f32 v101, v217, v218
	v_cvt_pk_bf16_f32 v102, v223, v232
	v_cvt_pk_bf16_f32 v103, v64, v65
	v_cvt_pk_bf16_f32 v104, v66, v67
	v_cvt_pk_bf16_f32 v105, v105, v106
	v_cvt_pk_bf16_f32 v106, v107, v72
	v_cvt_pk_bf16_f32 v107, v73, v74
	s_add_u32 s34, s46, s16
	s_addc_u32 s35, s47, s17
	s_add_u32 s24, s34, 0x23808000
	s_addc_u32 s25, s35, 0
	s_add_u32 s54, s34, 0x2380a000
	s_addc_u32 s55, s35, 0
	s_add_u32 s42, s46, s20
	s_addc_u32 s43, s47, s21
	s_add_u32 s56, s42, 0x21884000
	s_addc_u32 s57, s43, 0
	s_lshl_b32 s92, s15, 14
	s_add_i32 s92, s92, s94
	s_mov_b32 m0, s92
	s_lshl_b32 s96, s15, 13
	global_load_lds_dwordx4 v249, s[24:25]
	s_addk_i32 s92, 0x400
	s_mov_b32 m0, s92
	s_add_i32 s96, s96, s95
	global_load_lds_dwordx4 v250, s[24:25]
	s_nop 0
	s_mov_b32 m0, s96
	s_nop 0
	global_load_lds_dwordx4 v251, s[56:57]
	s_andn2_b64 vcc, exec, s[2:3]
	s_cbranch_vccnz .LBB4_925
	s_mov_b64 s[2:3], s[8:9]
	global_store_dwordx2 v193, v[184:185], s[2:3] nt

; DI void finishSM(f32x16& p0, f32x16& p1, float alpha, float& l_reg, bf16x8& pa0, bf16x8& pa1, bf16x8& pa2, bf16x8& pa3) {
; #pragma unroll
;     for (int r = 0; r < 16; ++r) p1[r] = __builtin_amdgcn_exp2f(p1[r]);
;     float ps = 0;
; #pragma unroll
;     for (int r = 0; r < 16; ++r) ps += p0[r];
; #pragma unroll
;     for (int r = 0; r < 16; ++r) ps += p1[r];
;     { auto rr = __builtin_amdgcn_permlane32_swap(__float_as_uint(ps), __float_as_uint(ps), false, false); ps = __uint_as_float(rr[0]) + __uint_as_float(rr[1]); }
;     l_reg = l_reg * alpha + ps;
;     ...
;     AT_PK4(p0, 0, pa0); AT_PK4(p0, 8, pa1); AT_PK4(p1, 0, pa2); AT_PK4(p1, 8, pa3);
;     ...
; }
; DI void qkt(f32x16& p0, f32x16& p1, const char* Ks, const bf16x8* qr, const f32x16& negm, int r32, int hi) {
; #pragma unroll
;     for (int d0 = 0; d0 < 4; ++d0) { const int cb = (d0 * 16 + hi * 8) * 2;
;         const bf16x8 b0 = *reinterpret_cast<const bf16x8*>(Ks + AT_KSWZ(r32, cb));
;         const bf16x8 b1 = *reinterpret_cast<const bf16x8*>(Ks + AT_KSWZ(32 + r32, cb));
;         p0 = __builtin_amdgcn_mfma_f32_32x32x16_bf16(b0, qr[d0], d0 == 0 ? negm : p0, 0, 0, 0);
;         p1 = __builtin_amdgcn_mfma_f32_32x32x16_bf16(b1, qr[d0], d0 == 0 ? negm : p1, 0, 0, 0); }
; }
.LBB4_944:
	v_exp_f32_e32 v182, v128
	v_exp_f32_e32 v234, v129
	v_exp_f32_e32 v235, v130
	v_exp_f32_e32 v236, v131
	v_exp_f32_e32 v237, v132
	v_exp_f32_e32 v238, v133
	v_exp_f32_e32 v239, v134
	v_exp_f32_e32 v240, v135
	v_exp_f32_e32 v241, v136
	v_exp_f32_e32 v242, v137
	v_exp_f32_e32 v243, v138
	v_exp_f32_e32 v244, v139
	v_exp_f32_e32 v245, v140
	v_exp_f32_e32 v246, v141
	v_exp_f32_e32 v247, v142
	v_exp_f32_e32 v248, v143
	v_add_u32_e32 v101, s54, v208
	v_add_u32_e32 v102, s54, v209
	v_add_u32_e32 v103, s54, v210
	ds_read_b128 v[172:175], v101 offset:49152
	ds_read_b128 v[176:179], v101 offset:53248
	ds_read_b128 v[218:221], v102 offset:49152
	ds_read_b128 v[222:225], v102 offset:53248
	ds_read_b128 v[226:229], v103 offset:49152
	ds_read_b128 v[230:233], v103 offset:53248
	v_exp_f32_e32 v112, v112
	v_exp_f32_e32 v113, v113
	v_exp_f32_e32 v114, v114
	s_waitcnt lgkmcnt(7)
	v_mfma_f32_32x32x16_bf16 v[128:143], v[96:99], v[156:159], v[80:95]
	v_exp_f32_e32 v115, v115
	v_exp_f32_e32 v116, v116
	v_exp_f32_e32 v117, v117
	v_exp_f32_e32 v118, v118
	v_exp_f32_e32 v119, v119
	s_waitcnt lgkmcnt(6)
	v_mfma_f32_32x32x16_bf16 v[96:111], v[168:171], v[156:159], v[80:95]
	v_exp_f32_e32 v168, v120
	v_add_f32_e32 v120, 0, v182
	v_add_f32_e32 v120, v234, v120
	v_add_f32_e32 v120, v235, v120
	v_add_f32_e32 v120, v236, v120
	v_add_f32_e32 v120, v237, v120
	v_add_f32_e32 v120, v238, v120
	v_add_f32_e32 v120, v239, v120
	v_add_f32_e32 v120, v240, v120
	v_add_f32_e32 v120, v241, v120
	v_add_f32_e32 v120, v242, v120
	s_waitcnt lgkmcnt(5)
	v_mfma_f32_32x32x16_bf16 v[128:143], v[172:175], v[152:155], v[128:143]
	v_add_f32_e32 v120, v243, v120
	v_add_f32_e32 v120, v244, v120
	v_add_f32_e32 v120, v245, v120
	v_add_f32_e32 v120, v246, v120
	v_add_f32_e32 v120, v247, v120
	v_add_f32_e32 v120, v248, v120
	v_add_f32_e32 v120, v112, v120
	s_waitcnt lgkmcnt(4)
	v_mfma_f32_32x32x16_bf16 v[96:111], v[176:179], v[152:155], v[96:111]
	v_add_f32_e32 v120, v113, v120
	v_add_f32_e32 v120, v114, v120
	v_add_f32_e32 v120, v115, v120
	v_add_f32_e32 v120, v116, v120
	v_exp_f32_e32 v169, v121
	v_add_f32_e32 v120, v117, v120
	v_exp_f32_e32 v170, v122
	s_waitcnt lgkmcnt(3)
	v_mfma_f32_32x32x16_bf16 v[128:143], v[218:221], v[148:151], v[128:143]
	v_add_f32_e32 v120, v118, v120
	v_exp_f32_e32 v171, v123
	v_add_f32_e32 v120, v119, v120
	v_exp_f32_e32 v172, v124
	v_exp_f32_e32 v173, v125
	s_waitcnt lgkmcnt(2)
	v_mfma_f32_32x32x16_bf16 v[96:111], v[222:225], v[148:151], v[96:111]
	v_exp_f32_e32 v174, v126
	v_exp_f32_e32 v175, v127
	v_add_f32_e32 v120, v174, v120
	s_waitcnt lgkmcnt(1)
	v_mfma_f32_32x32x16_bf16 v[128:143], v[226:229], v[144:147], v[128:143]
	v_add_f32_e32 v217, v175, v120
	v_cvt_pk_bf16_f32 v120, v182, v234
	v_cvt_pk_bf16_f32 v121, v235, v236
	v_cvt_pk_bf16_f32 v122, v237, v238
	v_cvt_pk_bf16_f32 v123, v239, v240
	v_cvt_pk_bf16_f32 v124, v241, v242
	s_waitcnt lgkmcnt(0)
	v_mfma_f32_32x32x16_bf16 v[96:111], v[230:233], v[144:147], v[96:111]
	v_cvt_pk_bf16_f32 v125, v243, v244
	v_cvt_pk_bf16_f32 v126, v245, v246
	v_cvt_pk_bf16_f32 v127, v247, v248
	v_cvt_pk_bf16_f32 v112, v112, v113
	v_cvt_pk_bf16_f32 v113, v114, v115
	v_cvt_pk_bf16_f32 v114, v116, v117
	v_cvt_pk_bf16_f32 v115, v118, v119
	s_add_u32 s24, s34, 0x2380c000
	s_addc_u32 s25, s35, 0
	s_add_u32 s34, s34, 0x2380e000
	s_addc_u32 s35, s35, 0
	s_add_u32 s42, s42, 0x21886000
	s_addc_u32 s43, s43, 0
	s_lshl_b32 s92, s29, 14
	s_add_i32 s92, s92, s94
	s_mov_b32 m0, s92
	s_lshl_b32 s96, s29, 13
	global_load_lds_dwordx4 v249, s[24:25]
	s_addk_i32 s92, 0x400
	s_mov_b32 m0, s92
	s_add_i32 s96, s96, s95
	global_load_lds_dwordx4 v250, s[24:25]
	s_nop 0
	s_mov_b32 m0, s96
	s_nop 0
	global_load_lds_dwordx4 v251, s[42:43]
	s_nop 0
	s_and_b64 vcc, exec, s[2:3]
	s_cbranch_vccnz .LBB4_946
	s_mov_b64 s[2:3], s[8:9]
	global_store_dwordx2 v193, v[184:185], s[2:3] nt
